# adds: GEMM K-loops drop the compiler's duplicate lgkmcnt(0) after each pre-MFMA barrier and the back-to-back setprio 0/1 pair inside each MFMA block
# speedup vs baseline: 1.0049x; 1.0049x over previous
; #define PG8_GREAD(dst, u, par) do { _Pragma("unroll") for (int h_ = 0; h_ < 2; ++h_) _Pragma("unroll") for (int i_ = 0; i_ < 2; ++i_) { const int rl_ = 128 * h_ + grl[i_]; \
;         const int tk_ = *(const PG8_LAS int*)(gtab + (par) * 2048 + rl_ * 8); const unsigned tok_ = (rl_ < (u).rows) ? ((unsigned)tk_ >> 2) : 0u; dst[h_][i_] = tok_ * (unsigned)(K * 2) + gcb[i_]; } } while (0)
; #define PG8_STAGE(bufoff, gbase, voff) do { _Pragma("unroll") for (int _i = 0; _i < 2; ++_i) \
;         __builtin_amdgcn_global_load_lds((const unsigned*)((const char*)(gbase) + (voff)[_i]), (PG8_LAS unsigned*)(lds + (bufoff) + ldsw + _i * 8192), 16, 0, 0); } while (0)
; #define PG8_WAIT_V(n) asm volatile("s_waitcnt vmcnt(" #n ")" ::: "memory")
; template <class Epi, class Sched, bool ALIGN_EPI = false, bool SP2 = false, bool GATHER = false>
; __device__ __forceinline__ void gemm_phase(PG8_LAS unsigned char* lds, const Gemm g, const Sched& S, const Epi& E, const int2* gslot = nullptr, PG8_LAS unsigned char* gtab = nullptr) {
;     ...
;             const char* a1 = cA + (size_t)(t + 1) * kstep;
;             const char* a2 = last ? nA : cA + (size_t)(t + 2) * kstep; const char* b2 = last ? nB : cB + (size_t)(t + 2) * kstep;
;             const char* a3 = a2 + kstep; const char* b3 = b2 + kstep;
;             if (last && has_next) S.a_ready(nxt);
;             if constexpr (GATHER) { if (last) { if (has_next) { PG8_GREAD(vN, nxt, (ui + 1) & 1); } else { _Pragma("unroll") for (int h_ = 0; h_ < 2; ++h_) _Pragma("unroll") for (int i_ = 0; i_ < 2; ++i_) vN[h_][i_] = vC[h_][i_]; } } }
;             unsigned vS[2][2];
; #pragma unroll
;             for (int h_ = 0; h_ < 2; ++h_)
; #pragma unroll
;                 for (int i_ = 0; i_ < 2; ++i_) vS[h_][i_] = (GATHER && last) ? vN[h_][i_] : vC[h_][i_];
;             if constexpr (SP2) {
;             PG8_LDB(B0, 0, 0); PG8_LDB(B1, 0, 1); PG8_SCHED; PG8_LDA(At, 0, 0); PG8_STAGE(PG8_SA(1, 1), a1 + PG8_AH(1), PG8_VA(vC, 1));
;             PG8_WAIT_V(8); PG8_WAIT_L(0); PG8_BAR; PG8_MMA(0, 0, At, B0); PG8_MMA(0, 1, At, B1); PG8_BAR; PG8_SCHED;
;             PG8_LDA(At, 0, 1); PG8_STAGE(PG8_SB(0, 0), b2, voffB); PG8_STAGE(PG8_SB(0, 1), b2 + hstep, voffB); PG8_STAGE(PG8_SA(0, 0), a2, PG8_VA(vS, 0));
;             PG8_WAIT_V(8); PG8_WAIT_L(0); PG8_BAR; PG8_MMA(1, 0, At, B0); PG8_MMA(1, 1, At, B1); PG8_BAR; PG8_SCHED;
.LBB0_131:
	s_add_u32 s2, s8, 0xfffc0080
	s_addc_u32 s10, s9, -1
	s_cmp_eq_u32 s34, 12
	s_cselect_b32 s27, s21, s10
	s_cselect_b32 s26, s28, s2
	s_cselect_b32 s11, s19, s31
	s_cselect_b32 s10, s29, s30
	s_add_i32 s2, 0, 0x10000
	v_add_u32_e32 v0, s2, v143
	s_add_i32 s35, 0, 0x14000
	ds_read_b128 v[146:149], v0
	ds_read_b128 v[150:153], v0 offset:1024
	ds_read_b128 v[154:157], v0 offset:2048
	ds_read_b128 v[158:161], v0 offset:3072
	v_add_u32_e32 v0, s35, v143
	ds_read_b128 v[162:165], v0
	ds_read_b128 v[166:169], v0 offset:1024
	ds_read_b128 v[170:173], v0 offset:2048
	ds_read_b128 v[174:177], v0 offset:3072
	v_lshl_add_u64 v[210:211], s[8:9], 0, v[138:139]
	s_add_i32 m0, s46, 0xc000
	ds_read_b128 v[178:181], v145
	ds_read_b128 v[182:185], v145 offset:1024
	ds_read_b128 v[186:189], v145 offset:2048
	ds_read_b128 v[190:193], v145 offset:3072
	ds_read_b128 v[194:197], v145 offset:4096
	ds_read_b128 v[198:201], v145 offset:5120
	ds_read_b128 v[202:205], v145 offset:6144
	ds_read_b128 v[206:209], v145 offset:7168
	global_load_lds_dwordx4 v[210:211], off
	v_lshl_add_u64 v[210:211], s[8:9], 0, v[140:141]
	s_add_i32 m0, s46, 0xe000
	s_nop 0
	global_load_lds_dwordx4 v[210:211], off
	s_waitcnt vmcnt(8)
	s_waitcnt lgkmcnt(0)
	s_barrier
	s_setprio 1
	v_mfma_f32_16x16x32_bf16 v[126:129], v[146:149], v[178:181], v[126:129]
	v_mfma_f32_16x16x32_bf16 v[122:125], v[154:157], v[178:181], v[122:125]
	v_mfma_f32_16x16x32_bf16 v[118:121], v[146:149], v[186:189], v[118:121]
	v_mfma_f32_16x16x32_bf16 v[114:117], v[154:157], v[186:189], v[114:117]
	v_mfma_f32_16x16x32_bf16 v[110:113], v[146:149], v[194:197], v[110:113]
	v_mfma_f32_16x16x32_bf16 v[106:109], v[154:157], v[194:197], v[106:109]
	v_mfma_f32_16x16x32_bf16 v[102:105], v[146:149], v[202:205], v[102:105]
	v_mfma_f32_16x16x32_bf16 v[98:101], v[154:157], v[202:205], v[98:101]
	v_mfma_f32_16x16x32_bf16 v[126:129], v[150:153], v[182:185], v[126:129]
	v_mfma_f32_16x16x32_bf16 v[122:125], v[158:161], v[182:185], v[122:125]
	v_mfma_f32_16x16x32_bf16 v[118:121], v[150:153], v[190:193], v[118:121]
	v_mfma_f32_16x16x32_bf16 v[114:117], v[158:161], v[190:193], v[114:117]
	v_mfma_f32_16x16x32_bf16 v[110:113], v[150:153], v[198:201], v[110:113]
	v_mfma_f32_16x16x32_bf16 v[106:109], v[158:161], v[198:201], v[106:109]
	v_mfma_f32_16x16x32_bf16 v[102:105], v[150:153], v[206:209], v[102:105]
	v_mfma_f32_16x16x32_bf16 v[98:101], v[158:161], v[206:209], v[98:101]
	v_mfma_f32_16x16x32_bf16 v[62:65], v[162:165], v[178:181], v[62:65]
	v_mfma_f32_16x16x32_bf16 v[58:61], v[170:173], v[178:181], v[58:61]
	v_mfma_f32_16x16x32_bf16 v[54:57], v[162:165], v[186:189], v[54:57]
	v_mfma_f32_16x16x32_bf16 v[50:53], v[170:173], v[186:189], v[50:53]
	v_mfma_f32_16x16x32_bf16 v[46:49], v[162:165], v[194:197], v[46:49]
	v_mfma_f32_16x16x32_bf16 v[42:45], v[170:173], v[194:197], v[42:45]
	v_mfma_f32_16x16x32_bf16 v[38:41], v[162:165], v[202:205], v[38:41]
	v_mfma_f32_16x16x32_bf16 v[34:37], v[170:173], v[202:205], v[34:37]
	v_mfma_f32_16x16x32_bf16 v[62:65], v[166:169], v[182:185], v[62:65]
	v_mfma_f32_16x16x32_bf16 v[58:61], v[174:177], v[182:185], v[58:61]
	v_mfma_f32_16x16x32_bf16 v[54:57], v[166:169], v[190:193], v[54:57]
	v_mfma_f32_16x16x32_bf16 v[50:53], v[174:177], v[190:193], v[50:53]
	v_mfma_f32_16x16x32_bf16 v[46:49], v[166:169], v[198:201], v[46:49]
	v_mfma_f32_16x16x32_bf16 v[42:45], v[174:177], v[198:201], v[42:45]
	v_mfma_f32_16x16x32_bf16 v[38:41], v[166:169], v[206:209], v[38:41]
	v_mfma_f32_16x16x32_bf16 v[34:37], v[174:177], v[206:209], v[34:37]
	s_setprio 0
	s_barrier
	s_add_i32 s2, s2, s45
	v_lshl_add_u64 v[210:211], s[10:11], 0, v[134:135]
	s_mov_b32 m0, s2
	ds_read_b128 v[178:181], v145 offset:16384
	ds_read_b128 v[182:185], v145 offset:17408
	ds_read_b128 v[186:189], v145 offset:18432
	ds_read_b128 v[190:193], v145 offset:19456
	ds_read_b128 v[194:197], v145 offset:20480
	ds_read_b128 v[198:201], v145 offset:21504
	ds_read_b128 v[202:205], v145 offset:22528
	ds_read_b128 v[206:209], v145 offset:23552
	global_load_lds_dwordx4 v[210:211], off
	s_add_i32 m0, s2, 0x2000
	s_add_u32 s36, s10, 0x40000
	v_lshl_add_u64 v[212:213], s[10:11], 0, v[130:131]
	s_addc_u32 s37, s11, 0
	s_add_i32 s2, s35, s45
	global_load_lds_dwordx4 v[212:213], off
	v_lshl_add_u64 v[214:215], s[36:37], 0, v[134:135]
	s_mov_b32 m0, s2
	v_lshl_add_u64 v[216:217], s[26:27], 0, v[132:133]
	global_load_lds_dwordx4 v[214:215], off
	v_lshl_add_u64 v[214:215], s[36:37], 0, v[130:131]
	s_add_i32 m0, s2, 0x2000
	s_nop 0
	global_load_lds_dwordx4 v[214:215], off
	v_lshl_add_u64 v[214:215], s[26:27], 0, v[136:137]
	s_mov_b32 m0, s46
	s_nop 0
	global_load_lds_dwordx4 v[214:215], off
	s_mov_b32 m0, s47
	s_nop 0
	global_load_lds_dwordx4 v[216:217], off
	s_waitcnt vmcnt(8)
	s_waitcnt lgkmcnt(0)
	s_barrier
; #define PG8_STAGE(bufoff, gbase, voff) do { _Pragma("unroll") for (int _i = 0; _i < 2; ++_i) \
;         __builtin_amdgcn_global_load_lds((const unsigned*)((const char*)(gbase) + (voff)[_i]), (PG8_LAS unsigned*)(lds + (bufoff) + ldsw + _i * 8192), 16, 0, 0); } while (0)
; #define PG8_LDA(dst, b, h) do { _Pragma("unroll") for (int m = 0; m < 4; ++m) _Pragma("unroll") for (int k = 0; k < 2; ++k) dst[m][k] = *(const PG8_LAS bf16x8*)(lds + PG8_SA(b, h) + aoff + m * 2048 + k * 1024); } while (0)
; #define PG8_LDB(dst, b, h) do { _Pragma("unroll") for (int n = 0; n < 2; ++n) _Pragma("unroll") for (int k = 0; k < 2; ++k) dst[n][k] = *(const PG8_LAS bf16x8*)(lds + PG8_SB(b, h) + boff + n * 2048 + k * 1024); } while (0)
; #define PG8_MMA(ai, bj, At, Bt) do { __builtin_amdgcn_s_setprio(1); _Pragma("unroll") for (int m = 0; m < 4; ++m) _Pragma("unroll") for (int n = 0; n < 2; ++n) _Pragma("unroll") for (int k = 0; k < 2; ++k) \
;         acc[ai][bj][m][n] = __builtin_amdgcn_mfma_f32_16x16x32_bf16(Bt[n][k], At[m][k], acc[ai][bj][m][n], 0, 0, 0); __builtin_amdgcn_s_setprio(0); } while (0)
; #define PG8_WAIT_V(n) asm volatile("s_waitcnt vmcnt(" #n ")" ::: "memory")
; #define PG8_WAIT_L(n) asm volatile("s_waitcnt lgkmcnt(" #n ")" ::: "memory")
; #define PG8_BAR __builtin_amdgcn_s_barrier()
; #define PG8_SCHED __builtin_amdgcn_sched_barrier(0)
; template <class Epi, class Sched, bool ALIGN_EPI = false, bool SP2 = false, bool GATHER = false>
; __device__ __forceinline__ void gemm_phase(PG8_LAS unsigned char* lds, const Gemm g, const Sched& S, const Epi& E, const int2* gslot = nullptr, PG8_LAS unsigned char* gtab = nullptr) {
;     ...
;             PG8_WAIT_V(8); PG8_WAIT_L(0); PG8_BAR; PG8_MMA(1, 0, At, B0); PG8_MMA(1, 1, At, B1); PG8_BAR; PG8_SCHED;
;             PG8_LDB(B0, 1, 0); PG8_LDB(B1, 1, 1); PG8_SCHED; PG8_LDA(At, 1, 0); PG8_STAGE(PG8_SA(0, 1), a2 + PG8_AH(1), PG8_VA(vS, 1));
;             PG8_WAIT_V(8); PG8_WAIT_L(0); PG8_BAR; PG8_MMA(0, 0, At, B0); PG8_MMA(0, 1, At, B1); PG8_BAR; PG8_SCHED;
	s_setprio 1
	v_mfma_f32_16x16x32_bf16 v[94:97], v[146:149], v[178:181], v[94:97]
	v_mfma_f32_16x16x32_bf16 v[90:93], v[154:157], v[178:181], v[90:93]
	v_mfma_f32_16x16x32_bf16 v[86:89], v[146:149], v[186:189], v[86:89]
	v_mfma_f32_16x16x32_bf16 v[82:85], v[154:157], v[186:189], v[82:85]
	v_mfma_f32_16x16x32_bf16 v[78:81], v[146:149], v[194:197], v[78:81]
	v_mfma_f32_16x16x32_bf16 v[74:77], v[154:157], v[194:197], v[74:77]
	v_mfma_f32_16x16x32_bf16 v[70:73], v[146:149], v[202:205], v[70:73]
	v_mfma_f32_16x16x32_bf16 v[66:69], v[154:157], v[202:205], v[66:69]
	v_mfma_f32_16x16x32_bf16 v[94:97], v[150:153], v[182:185], v[94:97]
	v_mfma_f32_16x16x32_bf16 v[90:93], v[158:161], v[182:185], v[90:93]
	v_mfma_f32_16x16x32_bf16 v[86:89], v[150:153], v[190:193], v[86:89]
	v_mfma_f32_16x16x32_bf16 v[82:85], v[158:161], v[190:193], v[82:85]
	v_mfma_f32_16x16x32_bf16 v[78:81], v[150:153], v[198:201], v[78:81]
	v_mfma_f32_16x16x32_bf16 v[74:77], v[158:161], v[198:201], v[74:77]
	v_mfma_f32_16x16x32_bf16 v[70:73], v[150:153], v[206:209], v[70:73]
	v_mfma_f32_16x16x32_bf16 v[66:69], v[158:161], v[206:209], v[66:69]
	v_mfma_f32_16x16x32_bf16 v[30:33], v[162:165], v[178:181], v[30:33]
	v_mfma_f32_16x16x32_bf16 v[26:29], v[170:173], v[178:181], v[26:29]
	v_mfma_f32_16x16x32_bf16 v[22:25], v[162:165], v[186:189], v[22:25]
	v_mfma_f32_16x16x32_bf16 v[18:21], v[170:173], v[186:189], v[18:21]
	v_mfma_f32_16x16x32_bf16 v[14:17], v[162:165], v[194:197], v[14:17]
	v_mfma_f32_16x16x32_bf16 v[10:13], v[170:173], v[194:197], v[10:13]
	v_mfma_f32_16x16x32_bf16 v[6:9], v[162:165], v[202:205], v[6:9]
	v_mfma_f32_16x16x32_bf16 v[2:5], v[170:173], v[202:205], v[2:5]
	v_mfma_f32_16x16x32_bf16 v[30:33], v[166:169], v[182:185], v[30:33]
	v_mfma_f32_16x16x32_bf16 v[26:29], v[174:177], v[182:185], v[26:29]
	v_mfma_f32_16x16x32_bf16 v[22:25], v[166:169], v[190:193], v[22:25]
	v_mfma_f32_16x16x32_bf16 v[18:21], v[174:177], v[190:193], v[18:21]
	v_mfma_f32_16x16x32_bf16 v[14:17], v[166:169], v[198:201], v[14:17]
	v_mfma_f32_16x16x32_bf16 v[10:13], v[174:177], v[198:201], v[10:13]
	v_mfma_f32_16x16x32_bf16 v[6:9], v[166:169], v[206:209], v[6:9]
	v_mfma_f32_16x16x32_bf16 v[2:5], v[174:177], v[206:209], v[2:5]
	s_setprio 0
	s_barrier
	s_add_i32 s2, 0, 0x18000
	v_add_u32_e32 v0, s2, v143
	s_add_i32 s35, 0, 0x1c000
	ds_read_b128 v[146:149], v0
	ds_read_b128 v[150:153], v0 offset:1024
	ds_read_b128 v[154:157], v0 offset:2048
	ds_read_b128 v[158:161], v0 offset:3072
	v_add_u32_e32 v0, s35, v143
	ds_read_b128 v[162:165], v0
	ds_read_b128 v[166:169], v0 offset:1024
	ds_read_b128 v[170:173], v0 offset:2048
	ds_read_b128 v[174:177], v0 offset:3072
	s_add_u32 s26, s26, 0x40000
	s_addc_u32 s27, s27, 0
	s_mov_b32 m0, s50
	v_lshl_add_u64 v[218:219], s[26:27], 0, v[136:137]
	ds_read_b128 v[178:181], v145 offset:32768
	ds_read_b128 v[182:185], v145 offset:33792
	ds_read_b128 v[186:189], v145 offset:34816
	ds_read_b128 v[190:193], v145 offset:35840
	ds_read_b128 v[194:197], v145 offset:36864
	ds_read_b128 v[198:201], v145 offset:37888
	ds_read_b128 v[202:205], v145 offset:38912
	ds_read_b128 v[206:209], v145 offset:39936
	global_load_lds_dwordx4 v[218:219], off
	v_lshl_add_u64 v[218:219], s[26:27], 0, v[132:133]
	s_mov_b32 m0, s51
	s_nop 0
	global_load_lds_dwordx4 v[218:219], off
	s_waitcnt vmcnt(8)
	s_waitcnt lgkmcnt(0)
	s_barrier
	s_setprio 1
	v_mfma_f32_16x16x32_bf16 v[126:129], v[146:149], v[178:181], v[126:129]
	v_mfma_f32_16x16x32_bf16 v[122:125], v[154:157], v[178:181], v[122:125]
	v_mfma_f32_16x16x32_bf16 v[118:121], v[146:149], v[186:189], v[118:121]
	v_mfma_f32_16x16x32_bf16 v[114:117], v[154:157], v[186:189], v[114:117]
	v_mfma_f32_16x16x32_bf16 v[110:113], v[146:149], v[194:197], v[110:113]
	v_mfma_f32_16x16x32_bf16 v[106:109], v[154:157], v[194:197], v[106:109]
	v_mfma_f32_16x16x32_bf16 v[102:105], v[146:149], v[202:205], v[102:105]
	v_mfma_f32_16x16x32_bf16 v[98:101], v[154:157], v[202:205], v[98:101]
	v_mfma_f32_16x16x32_bf16 v[126:129], v[150:153], v[182:185], v[126:129]
	v_mfma_f32_16x16x32_bf16 v[122:125], v[158:161], v[182:185], v[122:125]
	v_mfma_f32_16x16x32_bf16 v[118:121], v[150:153], v[190:193], v[118:121]
	v_mfma_f32_16x16x32_bf16 v[114:117], v[158:161], v[190:193], v[114:117]
	v_mfma_f32_16x16x32_bf16 v[110:113], v[150:153], v[198:201], v[110:113]
	v_mfma_f32_16x16x32_bf16 v[106:109], v[158:161], v[198:201], v[106:109]
	v_mfma_f32_16x16x32_bf16 v[102:105], v[150:153], v[206:209], v[102:105]
	v_mfma_f32_16x16x32_bf16 v[98:101], v[158:161], v[206:209], v[98:101]
	v_mfma_f32_16x16x32_bf16 v[62:65], v[162:165], v[178:181], v[62:65]
	v_mfma_f32_16x16x32_bf16 v[58:61], v[170:173], v[178:181], v[58:61]
	v_mfma_f32_16x16x32_bf16 v[54:57], v[162:165], v[186:189], v[54:57]
	v_mfma_f32_16x16x32_bf16 v[50:53], v[170:173], v[186:189], v[50:53]
	v_mfma_f32_16x16x32_bf16 v[46:49], v[162:165], v[194:197], v[46:49]
	v_mfma_f32_16x16x32_bf16 v[42:45], v[170:173], v[194:197], v[42:45]
	v_mfma_f32_16x16x32_bf16 v[38:41], v[162:165], v[202:205], v[38:41]
	v_mfma_f32_16x16x32_bf16 v[34:37], v[170:173], v[202:205], v[34:37]
	v_mfma_f32_16x16x32_bf16 v[62:65], v[166:169], v[182:185], v[62:65]
	v_mfma_f32_16x16x32_bf16 v[58:61], v[174:177], v[182:185], v[58:61]
	v_mfma_f32_16x16x32_bf16 v[54:57], v[166:169], v[190:193], v[54:57]
	v_mfma_f32_16x16x32_bf16 v[50:53], v[174:177], v[190:193], v[50:53]
	v_mfma_f32_16x16x32_bf16 v[46:49], v[166:169], v[198:201], v[46:49]
	v_mfma_f32_16x16x32_bf16 v[42:45], v[174:177], v[198:201], v[42:45]
	v_mfma_f32_16x16x32_bf16 v[38:41], v[166:169], v[206:209], v[38:41]
	v_mfma_f32_16x16x32_bf16 v[34:37], v[174:177], v[206:209], v[34:37]
	s_setprio 0
	s_barrier
; #define PG8_STAGE(bufoff, gbase, voff) do { _Pragma("unroll") for (int _i = 0; _i < 2; ++_i) \
;         __builtin_amdgcn_global_load_lds((const unsigned*)((const char*)(gbase) + (voff)[_i]), (PG8_LAS unsigned*)(lds + (bufoff) + ldsw + _i * 8192), 16, 0, 0); } while (0)
; #define PG8_LDA(dst, b, h) do { _Pragma("unroll") for (int m = 0; m < 4; ++m) _Pragma("unroll") for (int k = 0; k < 2; ++k) dst[m][k] = *(const PG8_LAS bf16x8*)(lds + PG8_SA(b, h) + aoff + m * 2048 + k * 1024); } while (0)
; #define PG8_MMA(ai, bj, At, Bt) do { __builtin_amdgcn_s_setprio(1); _Pragma("unroll") for (int m = 0; m < 4; ++m) _Pragma("unroll") for (int n = 0; n < 2; ++n) _Pragma("unroll") for (int k = 0; k < 2; ++k) \
;         acc[ai][bj][m][n] = __builtin_amdgcn_mfma_f32_16x16x32_bf16(Bt[n][k], At[m][k], acc[ai][bj][m][n], 0, 0, 0); __builtin_amdgcn_s_setprio(0); } while (0)
; #define PG8_WAIT_V(n) asm volatile("s_waitcnt vmcnt(" #n ")" ::: "memory")
; #define PG8_WAIT_L(n) asm volatile("s_waitcnt lgkmcnt(" #n ")" ::: "memory")
; #define PG8_BAR __builtin_amdgcn_s_barrier()
; #define PG8_SCHED __builtin_amdgcn_sched_barrier(0)
; template <class Epi, class Sched, bool ALIGN_EPI = false, bool SP2 = false, bool GATHER = false>
; __device__ __forceinline__ void gemm_phase(PG8_LAS unsigned char* lds, const Gemm g, const Sched& S, const Epi& E, const int2* gslot = nullptr, PG8_LAS unsigned char* gtab = nullptr) {
;     ...
;             PG8_LDA(At, 1, 1); PG8_STAGE(PG8_SB(1, 0), b3, voffB); PG8_STAGE(PG8_SB(1, 1), b3 + hstep, voffB); PG8_STAGE(PG8_SA(1, 0), a3, PG8_VA(vS, 0));
;             PG8_WAIT_V(8); PG8_WAIT_L(0); PG8_BAR; PG8_MMA(1, 0, At, B0); PG8_MMA(1, 1, At, B1); PG8_BAR; PG8_SCHED;
;     ...
;         if constexpr (ALIGN_EPI) { if (wr == 0) PG8_BAR; }
	s_add_i32 s2, s2, s45
	v_lshl_add_u64 v[210:211], v[210:211], 0, s[54:55]
	s_mov_b32 m0, s2
	ds_read_b128 v[178:181], v145 offset:49152
	ds_read_b128 v[182:185], v145 offset:50176
	ds_read_b128 v[186:189], v145 offset:51200
	ds_read_b128 v[190:193], v145 offset:52224
	ds_read_b128 v[194:197], v145 offset:53248
	ds_read_b128 v[198:201], v145 offset:54272
	ds_read_b128 v[202:205], v145 offset:55296
	ds_read_b128 v[206:209], v145 offset:56320
	global_load_lds_dwordx4 v[210:211], off
	s_add_i32 m0, s2, 0x2000
	s_add_u32 s10, s10, 0x40080
	v_lshl_add_u64 v[210:211], v[212:213], 0, s[54:55]
	s_addc_u32 s11, s11, 0
	s_add_i32 s2, s35, s45
	global_load_lds_dwordx4 v[210:211], off
	v_lshl_add_u64 v[210:211], s[10:11], 0, v[134:135]
	s_mov_b32 m0, s2
	s_nop 0
	global_load_lds_dwordx4 v[210:211], off
	v_lshl_add_u64 v[210:211], s[10:11], 0, v[130:131]
	s_add_i32 m0, s2, 0x2000
	s_nop 0
	global_load_lds_dwordx4 v[210:211], off
	v_lshl_add_u64 v[210:211], v[214:215], 0, s[54:55]
	s_mov_b32 m0, s60
	s_nop 0
	global_load_lds_dwordx4 v[210:211], off
	v_lshl_add_u64 v[210:211], v[216:217], 0, s[54:55]
	s_mov_b32 m0, s61
	s_nop 0
	global_load_lds_dwordx4 v[210:211], off
	s_waitcnt vmcnt(8)
	s_waitcnt lgkmcnt(0)
	s_barrier
	s_setprio 1
	v_mfma_f32_16x16x32_bf16 v[94:97], v[146:149], v[178:181], v[94:97]
	v_mfma_f32_16x16x32_bf16 v[90:93], v[154:157], v[178:181], v[90:93]
	v_mfma_f32_16x16x32_bf16 v[86:89], v[146:149], v[186:189], v[86:89]
	v_mfma_f32_16x16x32_bf16 v[82:85], v[154:157], v[186:189], v[82:85]
	v_mfma_f32_16x16x32_bf16 v[78:81], v[146:149], v[194:197], v[78:81]
	v_mfma_f32_16x16x32_bf16 v[74:77], v[154:157], v[194:197], v[74:77]
	v_mfma_f32_16x16x32_bf16 v[70:73], v[146:149], v[202:205], v[70:73]
	v_mfma_f32_16x16x32_bf16 v[66:69], v[154:157], v[202:205], v[66:69]
	v_mfma_f32_16x16x32_bf16 v[94:97], v[150:153], v[182:185], v[94:97]
	v_mfma_f32_16x16x32_bf16 v[90:93], v[158:161], v[182:185], v[90:93]
	v_mfma_f32_16x16x32_bf16 v[86:89], v[150:153], v[190:193], v[86:89]
	v_mfma_f32_16x16x32_bf16 v[82:85], v[158:161], v[190:193], v[82:85]
	v_mfma_f32_16x16x32_bf16 v[78:81], v[150:153], v[198:201], v[78:81]
	v_mfma_f32_16x16x32_bf16 v[74:77], v[158:161], v[198:201], v[74:77]
	v_mfma_f32_16x16x32_bf16 v[70:73], v[150:153], v[206:209], v[70:73]
	v_mfma_f32_16x16x32_bf16 v[66:69], v[158:161], v[206:209], v[66:69]
	v_mfma_f32_16x16x32_bf16 v[30:33], v[162:165], v[178:181], v[30:33]
	v_mfma_f32_16x16x32_bf16 v[26:29], v[170:173], v[178:181], v[26:29]
	v_mfma_f32_16x16x32_bf16 v[22:25], v[162:165], v[186:189], v[22:25]
	v_mfma_f32_16x16x32_bf16 v[18:21], v[170:173], v[186:189], v[18:21]
	v_mfma_f32_16x16x32_bf16 v[14:17], v[162:165], v[194:197], v[14:17]
	v_mfma_f32_16x16x32_bf16 v[10:13], v[170:173], v[194:197], v[10:13]
	v_mfma_f32_16x16x32_bf16 v[6:9], v[162:165], v[202:205], v[6:9]
	v_mfma_f32_16x16x32_bf16 v[2:5], v[170:173], v[202:205], v[2:5]
	v_mfma_f32_16x16x32_bf16 v[30:33], v[166:169], v[182:185], v[30:33]
	v_mfma_f32_16x16x32_bf16 v[26:29], v[174:177], v[182:185], v[26:29]
	v_mfma_f32_16x16x32_bf16 v[22:25], v[166:169], v[190:193], v[22:25]
	v_mfma_f32_16x16x32_bf16 v[18:21], v[174:177], v[190:193], v[18:21]
	v_mfma_f32_16x16x32_bf16 v[14:17], v[166:169], v[198:201], v[14:17]
	v_mfma_f32_16x16x32_bf16 v[10:13], v[174:177], v[198:201], v[10:13]
	v_mfma_f32_16x16x32_bf16 v[6:9], v[166:169], v[206:209], v[6:9]
	v_mfma_f32_16x16x32_bf16 v[2:5], v[174:177], v[206:209], v[2:5]
	s_setprio 0
	s_barrier
	s_add_i32 s34, s34, 2
	s_add_u32 s8, s8, 0x100
	s_addc_u32 s9, s9, 0
	s_add_u32 s30, s30, 0x100
	s_addc_u32 s31, s31, 0
	s_cmp_gt_u32 s34, 13
	s_cbranch_scc0 .LBB0_131
	s_and_b64 vcc, exec, s[14:15]
	s_cbranch_vccz .LBB0_134
	s_barrier

; #define PG8_GREAD(dst, u, par) do { _Pragma("unroll") for (int h_ = 0; h_ < 2; ++h_) _Pragma("unroll") for (int i_ = 0; i_ < 2; ++i_) { const int rl_ = 128 * h_ + grl[i_]; \
;         const int tk_ = *(const PG8_LAS int*)(gtab + (par) * 2048 + rl_ * 8); const unsigned tok_ = (rl_ < (u).rows) ? ((unsigned)tk_ >> 2) : 0u; dst[h_][i_] = tok_ * (unsigned)(K * 2) + gcb[i_]; } } while (0)
; #define PG8_STAGE(bufoff, gbase, voff) do { _Pragma("unroll") for (int _i = 0; _i < 2; ++_i) \
;         __builtin_amdgcn_global_load_lds((const unsigned*)((const char*)(gbase) + (voff)[_i]), (PG8_LAS unsigned*)(lds + (bufoff) + ldsw + _i * 8192), 16, 0, 0); } while (0)
; #define PG8_WAIT_V(n) asm volatile("s_waitcnt vmcnt(" #n ")" ::: "memory")
; template <class Epi, class Sched, bool ALIGN_EPI = false, bool SP2 = false, bool GATHER = false>
; __device__ __forceinline__ void gemm_phase(PG8_LAS unsigned char* lds, const Gemm g, const Sched& S, const Epi& E, const int2* gslot = nullptr, PG8_LAS unsigned char* gtab = nullptr) {
;     ...
;             const char* a1 = cA + (size_t)(t + 1) * kstep;
;             const char* a2 = last ? nA : cA + (size_t)(t + 2) * kstep; const char* b2 = last ? nB : cB + (size_t)(t + 2) * kstep;
;             const char* a3 = a2 + kstep; const char* b3 = b2 + kstep;
;             if (last && has_next) S.a_ready(nxt);
;             if constexpr (GATHER) { if (last) { if (has_next) { PG8_GREAD(vN, nxt, (ui + 1) & 1); } else { _Pragma("unroll") for (int h_ = 0; h_ < 2; ++h_) _Pragma("unroll") for (int i_ = 0; i_ < 2; ++i_) vN[h_][i_] = vC[h_][i_]; } } }
;             unsigned vS[2][2];
; #pragma unroll
;             for (int h_ = 0; h_ < 2; ++h_)
; #pragma unroll
;                 for (int i_ = 0; i_ < 2; ++i_) vS[h_][i_] = (GATHER && last) ? vN[h_][i_] : vC[h_][i_];
;             if constexpr (SP2) {
;             PG8_LDB(B0, 0, 0); PG8_LDB(B1, 0, 1); PG8_SCHED; PG8_LDA(At, 0, 0); PG8_STAGE(PG8_SA(1, 1), a1 + PG8_AH(1), PG8_VA(vC, 1));
;             PG8_WAIT_V(8); PG8_WAIT_L(0); PG8_BAR; PG8_MMA(0, 0, At, B0); PG8_MMA(0, 1, At, B1); PG8_BAR; PG8_SCHED;
;             PG8_LDA(At, 0, 1); PG8_STAGE(PG8_SB(0, 0), b2, voffB); PG8_STAGE(PG8_SB(0, 1), b2 + hstep, voffB); PG8_STAGE(PG8_SA(0, 0), a2, PG8_VA(vS, 0));
;             PG8_WAIT_V(8); PG8_WAIT_L(0); PG8_BAR; PG8_MMA(1, 0, At, B0); PG8_MMA(1, 1, At, B1); PG8_BAR; PG8_SCHED;
.LBB0_482:
	s_add_u32 s34, s30, 0x100
	s_addc_u32 s35, s31, 0
	s_cmp_eq_u32 s66, 28
	s_cselect_b32 s39, s25, s35
	s_cselect_b32 s38, s62, s34
	s_cselect_b32 s37, s23, s65
	s_cselect_b32 s36, s63, s64
	s_add_i32 s2, 0, 0x10000
	s_add_i32 s67, 0, 0x14000
	v_add_u32_e32 v148, s2, v215
	v_add_u32_e32 v164, s67, v215
	ds_read_b128 v[136:139], v148
	ds_read_b128 v[140:143], v148 offset:1024
	ds_read_b128 v[144:147], v148 offset:2048
	ds_read_b128 v[148:151], v148 offset:3072
	ds_read_b128 v[152:155], v164
	ds_read_b128 v[156:159], v164 offset:1024
	ds_read_b128 v[160:163], v164 offset:2048
	ds_read_b128 v[164:167], v164 offset:3072
	v_lshl_add_u64 v[202:203], s[30:31], 0, v[132:133]
	s_add_i32 m0, s46, 0xc000
	ds_read_b128 v[168:171], v181
	ds_read_b128 v[172:175], v181 offset:1024
	ds_read_b128 v[176:179], v181 offset:2048
	ds_read_b128 v[182:185], v181 offset:3072
	ds_read_b128 v[186:189], v181 offset:4096
	ds_read_b128 v[190:193], v181 offset:5120
	ds_read_b128 v[194:197], v181 offset:6144
	ds_read_b128 v[198:201], v181 offset:7168
	global_load_lds_dwordx4 v[202:203], off
	v_lshl_add_u64 v[202:203], s[30:31], 0, v[134:135]
	s_add_i32 m0, s46, 0xe000
	s_nop 0
	global_load_lds_dwordx4 v[202:203], off
	s_waitcnt vmcnt(8)
	s_waitcnt lgkmcnt(0)
	s_barrier
	s_setprio 1
	v_mfma_f32_16x16x32_bf16 v[126:129], v[136:139], v[168:171], v[126:129]
	v_mfma_f32_16x16x32_bf16 v[122:125], v[144:147], v[168:171], v[122:125]
	v_mfma_f32_16x16x32_bf16 v[110:113], v[136:139], v[176:179], v[110:113]
	v_mfma_f32_16x16x32_bf16 v[106:109], v[144:147], v[176:179], v[106:109]
	v_mfma_f32_16x16x32_bf16 v[94:97], v[136:139], v[186:189], v[94:97]
	v_mfma_f32_16x16x32_bf16 v[90:93], v[144:147], v[186:189], v[90:93]
	v_mfma_f32_16x16x32_bf16 v[78:81], v[136:139], v[194:197], v[78:81]
	v_mfma_f32_16x16x32_bf16 v[74:77], v[144:147], v[194:197], v[74:77]
	v_mfma_f32_16x16x32_bf16 v[126:129], v[140:143], v[172:175], v[126:129]
	v_mfma_f32_16x16x32_bf16 v[122:125], v[148:151], v[172:175], v[122:125]
	v_mfma_f32_16x16x32_bf16 v[110:113], v[140:143], v[182:185], v[110:113]
	v_mfma_f32_16x16x32_bf16 v[106:109], v[148:151], v[182:185], v[106:109]
	v_mfma_f32_16x16x32_bf16 v[94:97], v[140:143], v[190:193], v[94:97]
	v_mfma_f32_16x16x32_bf16 v[90:93], v[148:151], v[190:193], v[90:93]
	v_mfma_f32_16x16x32_bf16 v[78:81], v[140:143], v[198:201], v[78:81]
	v_mfma_f32_16x16x32_bf16 v[74:77], v[148:151], v[198:201], v[74:77]
	v_mfma_f32_16x16x32_bf16 v[118:121], v[152:155], v[168:171], v[118:121]
	v_mfma_f32_16x16x32_bf16 v[114:117], v[160:163], v[168:171], v[114:117]
	v_mfma_f32_16x16x32_bf16 v[102:105], v[152:155], v[176:179], v[102:105]
	v_mfma_f32_16x16x32_bf16 v[98:101], v[160:163], v[176:179], v[98:101]
	v_mfma_f32_16x16x32_bf16 v[86:89], v[152:155], v[186:189], v[86:89]
	v_mfma_f32_16x16x32_bf16 v[82:85], v[160:163], v[186:189], v[82:85]
	v_mfma_f32_16x16x32_bf16 v[70:73], v[152:155], v[194:197], v[70:73]
	v_mfma_f32_16x16x32_bf16 v[66:69], v[160:163], v[194:197], v[66:69]
	v_mfma_f32_16x16x32_bf16 v[118:121], v[156:159], v[172:175], v[118:121]
	v_mfma_f32_16x16x32_bf16 v[114:117], v[164:167], v[172:175], v[114:117]
	v_mfma_f32_16x16x32_bf16 v[102:105], v[156:159], v[182:185], v[102:105]
	v_mfma_f32_16x16x32_bf16 v[98:101], v[164:167], v[182:185], v[98:101]
	v_mfma_f32_16x16x32_bf16 v[86:89], v[156:159], v[190:193], v[86:89]
	v_mfma_f32_16x16x32_bf16 v[82:85], v[164:167], v[190:193], v[82:85]
	v_mfma_f32_16x16x32_bf16 v[70:73], v[156:159], v[198:201], v[70:73]
	v_mfma_f32_16x16x32_bf16 v[66:69], v[164:167], v[198:201], v[66:69]
	s_setprio 0
	s_barrier
	s_add_i32 s2, s2, s45
	v_lshl_add_u64 v[202:203], s[36:37], 0, v[0:1]
	s_mov_b32 m0, s2
	ds_read_b128 v[168:171], v181 offset:16384
	ds_read_b128 v[172:175], v181 offset:17408
	ds_read_b128 v[176:179], v181 offset:18432
	ds_read_b128 v[182:185], v181 offset:19456
	ds_read_b128 v[186:189], v181 offset:20480
	ds_read_b128 v[190:193], v181 offset:21504
	ds_read_b128 v[194:197], v181 offset:22528
	ds_read_b128 v[198:201], v181 offset:23552
	global_load_lds_dwordx4 v[202:203], off
	s_add_i32 m0, s2, 0x2000
	s_add_u32 s30, s36, 0x80000
	v_lshl_add_u64 v[204:205], s[36:37], 0, v[130:131]
	s_addc_u32 s31, s37, 0
	s_add_i32 s2, s67, s45
	global_load_lds_dwordx4 v[204:205], off
	v_lshl_add_u64 v[206:207], s[30:31], 0, v[0:1]
	s_mov_b32 m0, s2
	v_lshl_add_u64 v[208:209], s[38:39], 0, v[130:131]
	global_load_lds_dwordx4 v[206:207], off
	v_lshl_add_u64 v[206:207], s[30:31], 0, v[130:131]
	s_add_i32 m0, s2, 0x2000
	s_nop 0
	global_load_lds_dwordx4 v[206:207], off
	v_lshl_add_u64 v[206:207], s[38:39], 0, v[0:1]
	s_mov_b32 m0, s46
	s_nop 0
	global_load_lds_dwordx4 v[206:207], off
	s_mov_b32 m0, s47
	s_nop 0
	global_load_lds_dwordx4 v[208:209], off
	s_waitcnt vmcnt(8)
	s_waitcnt lgkmcnt(0)
	s_barrier
; #define PG8_STAGE(bufoff, gbase, voff) do { _Pragma("unroll") for (int _i = 0; _i < 2; ++_i) \
;         __builtin_amdgcn_global_load_lds((const unsigned*)((const char*)(gbase) + (voff)[_i]), (PG8_LAS unsigned*)(lds + (bufoff) + ldsw + _i * 8192), 16, 0, 0); } while (0)
; #define PG8_LDA(dst, b, h) do { _Pragma("unroll") for (int m = 0; m < 4; ++m) _Pragma("unroll") for (int k = 0; k < 2; ++k) dst[m][k] = *(const PG8_LAS bf16x8*)(lds + PG8_SA(b, h) + aoff + m * 2048 + k * 1024); } while (0)
; #define PG8_LDB(dst, b, h) do { _Pragma("unroll") for (int n = 0; n < 2; ++n) _Pragma("unroll") for (int k = 0; k < 2; ++k) dst[n][k] = *(const PG8_LAS bf16x8*)(lds + PG8_SB(b, h) + boff + n * 2048 + k * 1024); } while (0)
; #define PG8_MMA(ai, bj, At, Bt) do { __builtin_amdgcn_s_setprio(1); _Pragma("unroll") for (int m = 0; m < 4; ++m) _Pragma("unroll") for (int n = 0; n < 2; ++n) _Pragma("unroll") for (int k = 0; k < 2; ++k) \
;         acc[ai][bj][m][n] = __builtin_amdgcn_mfma_f32_16x16x32_bf16(Bt[n][k], At[m][k], acc[ai][bj][m][n], 0, 0, 0); __builtin_amdgcn_s_setprio(0); } while (0)
; #define PG8_WAIT_V(n) asm volatile("s_waitcnt vmcnt(" #n ")" ::: "memory")
; #define PG8_WAIT_L(n) asm volatile("s_waitcnt lgkmcnt(" #n ")" ::: "memory")
; #define PG8_BAR __builtin_amdgcn_s_barrier()
; #define PG8_SCHED __builtin_amdgcn_sched_barrier(0)
; template <class Epi, class Sched, bool ALIGN_EPI = false, bool SP2 = false, bool GATHER = false>
; __device__ __forceinline__ void gemm_phase(PG8_LAS unsigned char* lds, const Gemm g, const Sched& S, const Epi& E, const int2* gslot = nullptr, PG8_LAS unsigned char* gtab = nullptr) {
;     ...
;             PG8_WAIT_V(8); PG8_WAIT_L(0); PG8_BAR; PG8_MMA(1, 0, At, B0); PG8_MMA(1, 1, At, B1); PG8_BAR; PG8_SCHED;
;             PG8_LDB(B0, 1, 0); PG8_LDB(B1, 1, 1); PG8_SCHED; PG8_LDA(At, 1, 0); PG8_STAGE(PG8_SA(0, 1), a2 + PG8_AH(1), PG8_VA(vS, 1));
;             PG8_WAIT_V(8); PG8_WAIT_L(0); PG8_BAR; PG8_MMA(0, 0, At, B0); PG8_MMA(0, 1, At, B1); PG8_BAR; PG8_SCHED;
	s_setprio 1
	v_mfma_f32_16x16x32_bf16 v[62:65], v[136:139], v[168:171], v[62:65]
	v_mfma_f32_16x16x32_bf16 v[58:61], v[144:147], v[168:171], v[58:61]
	v_mfma_f32_16x16x32_bf16 v[46:49], v[136:139], v[176:179], v[46:49]
	v_mfma_f32_16x16x32_bf16 v[42:45], v[144:147], v[176:179], v[42:45]
	v_mfma_f32_16x16x32_bf16 v[30:33], v[136:139], v[186:189], v[30:33]
	v_mfma_f32_16x16x32_bf16 v[26:29], v[144:147], v[186:189], v[26:29]
	v_mfma_f32_16x16x32_bf16 v[14:17], v[136:139], v[194:197], v[14:17]
	v_mfma_f32_16x16x32_bf16 v[10:13], v[144:147], v[194:197], v[10:13]
	v_mfma_f32_16x16x32_bf16 v[62:65], v[140:143], v[172:175], v[62:65]
	v_mfma_f32_16x16x32_bf16 v[58:61], v[148:151], v[172:175], v[58:61]
	v_mfma_f32_16x16x32_bf16 v[46:49], v[140:143], v[182:185], v[46:49]
	v_mfma_f32_16x16x32_bf16 v[42:45], v[148:151], v[182:185], v[42:45]
	v_mfma_f32_16x16x32_bf16 v[30:33], v[140:143], v[190:193], v[30:33]
	v_mfma_f32_16x16x32_bf16 v[26:29], v[148:151], v[190:193], v[26:29]
	v_mfma_f32_16x16x32_bf16 v[14:17], v[140:143], v[198:201], v[14:17]
	v_mfma_f32_16x16x32_bf16 v[10:13], v[148:151], v[198:201], v[10:13]
	v_mfma_f32_16x16x32_bf16 v[54:57], v[152:155], v[168:171], v[54:57]
	v_mfma_f32_16x16x32_bf16 v[50:53], v[160:163], v[168:171], v[50:53]
	v_mfma_f32_16x16x32_bf16 v[38:41], v[152:155], v[176:179], v[38:41]
	v_mfma_f32_16x16x32_bf16 v[34:37], v[160:163], v[176:179], v[34:37]
	v_mfma_f32_16x16x32_bf16 v[22:25], v[152:155], v[186:189], v[22:25]
	v_mfma_f32_16x16x32_bf16 v[18:21], v[160:163], v[186:189], v[18:21]
	v_mfma_f32_16x16x32_bf16 v[6:9], v[152:155], v[194:197], v[6:9]
	v_mfma_f32_16x16x32_bf16 v[2:5], v[160:163], v[194:197], v[2:5]
	v_mfma_f32_16x16x32_bf16 v[54:57], v[156:159], v[172:175], v[54:57]
	v_mfma_f32_16x16x32_bf16 v[50:53], v[164:167], v[172:175], v[50:53]
	v_mfma_f32_16x16x32_bf16 v[38:41], v[156:159], v[182:185], v[38:41]
	v_mfma_f32_16x16x32_bf16 v[34:37], v[164:167], v[182:185], v[34:37]
	v_mfma_f32_16x16x32_bf16 v[22:25], v[156:159], v[190:193], v[22:25]
	v_mfma_f32_16x16x32_bf16 v[18:21], v[164:167], v[190:193], v[18:21]
	v_mfma_f32_16x16x32_bf16 v[6:9], v[156:159], v[198:201], v[6:9]
	v_mfma_f32_16x16x32_bf16 v[2:5], v[164:167], v[198:201], v[2:5]
	s_setprio 0
	s_barrier
	s_add_i32 s2, 0, 0x18000
	s_add_i32 s67, 0, 0x1c000
	v_add_u32_e32 v148, s2, v215
	v_add_u32_e32 v164, s67, v215
	ds_read_b128 v[136:139], v148
	ds_read_b128 v[140:143], v148 offset:1024
	ds_read_b128 v[144:147], v148 offset:2048
	ds_read_b128 v[148:151], v148 offset:3072
	ds_read_b128 v[152:155], v164
	ds_read_b128 v[156:159], v164 offset:1024
	ds_read_b128 v[160:163], v164 offset:2048
	ds_read_b128 v[164:167], v164 offset:3072
	s_add_u32 s30, s38, 0x80000
	s_addc_u32 s31, s39, 0
	s_mov_b32 m0, s50
	v_lshl_add_u64 v[210:211], s[30:31], 0, v[0:1]
	ds_read_b128 v[168:171], v181 offset:32768
	ds_read_b128 v[172:175], v181 offset:33792
	ds_read_b128 v[176:179], v181 offset:34816
	ds_read_b128 v[182:185], v181 offset:35840
	ds_read_b128 v[186:189], v181 offset:36864
	ds_read_b128 v[190:193], v181 offset:37888
	ds_read_b128 v[194:197], v181 offset:38912
	ds_read_b128 v[198:201], v181 offset:39936
	global_load_lds_dwordx4 v[210:211], off
	v_lshl_add_u64 v[210:211], s[30:31], 0, v[130:131]
	s_mov_b32 m0, s51
	s_nop 0
	global_load_lds_dwordx4 v[210:211], off
	s_waitcnt vmcnt(8)
	s_waitcnt lgkmcnt(0)
	s_barrier
	s_setprio 1
	v_mfma_f32_16x16x32_bf16 v[126:129], v[136:139], v[168:171], v[126:129]
	v_mfma_f32_16x16x32_bf16 v[122:125], v[144:147], v[168:171], v[122:125]
	v_mfma_f32_16x16x32_bf16 v[110:113], v[136:139], v[176:179], v[110:113]
	v_mfma_f32_16x16x32_bf16 v[106:109], v[144:147], v[176:179], v[106:109]
	v_mfma_f32_16x16x32_bf16 v[94:97], v[136:139], v[186:189], v[94:97]
	v_mfma_f32_16x16x32_bf16 v[90:93], v[144:147], v[186:189], v[90:93]
	v_mfma_f32_16x16x32_bf16 v[78:81], v[136:139], v[194:197], v[78:81]
	v_mfma_f32_16x16x32_bf16 v[74:77], v[144:147], v[194:197], v[74:77]
	v_mfma_f32_16x16x32_bf16 v[126:129], v[140:143], v[172:175], v[126:129]
	v_mfma_f32_16x16x32_bf16 v[122:125], v[148:151], v[172:175], v[122:125]
	v_mfma_f32_16x16x32_bf16 v[110:113], v[140:143], v[182:185], v[110:113]
	v_mfma_f32_16x16x32_bf16 v[106:109], v[148:151], v[182:185], v[106:109]
	v_mfma_f32_16x16x32_bf16 v[94:97], v[140:143], v[190:193], v[94:97]
	v_mfma_f32_16x16x32_bf16 v[90:93], v[148:151], v[190:193], v[90:93]
	v_mfma_f32_16x16x32_bf16 v[78:81], v[140:143], v[198:201], v[78:81]
	v_mfma_f32_16x16x32_bf16 v[74:77], v[148:151], v[198:201], v[74:77]
	v_mfma_f32_16x16x32_bf16 v[118:121], v[152:155], v[168:171], v[118:121]
	v_mfma_f32_16x16x32_bf16 v[114:117], v[160:163], v[168:171], v[114:117]
	v_mfma_f32_16x16x32_bf16 v[102:105], v[152:155], v[176:179], v[102:105]
	v_mfma_f32_16x16x32_bf16 v[98:101], v[160:163], v[176:179], v[98:101]
	v_mfma_f32_16x16x32_bf16 v[86:89], v[152:155], v[186:189], v[86:89]
	v_mfma_f32_16x16x32_bf16 v[82:85], v[160:163], v[186:189], v[82:85]
	v_mfma_f32_16x16x32_bf16 v[70:73], v[152:155], v[194:197], v[70:73]
	v_mfma_f32_16x16x32_bf16 v[66:69], v[160:163], v[194:197], v[66:69]
	v_mfma_f32_16x16x32_bf16 v[118:121], v[156:159], v[172:175], v[118:121]
	v_mfma_f32_16x16x32_bf16 v[114:117], v[164:167], v[172:175], v[114:117]
	v_mfma_f32_16x16x32_bf16 v[102:105], v[156:159], v[182:185], v[102:105]
	v_mfma_f32_16x16x32_bf16 v[98:101], v[164:167], v[182:185], v[98:101]
	v_mfma_f32_16x16x32_bf16 v[86:89], v[156:159], v[190:193], v[86:89]
	v_mfma_f32_16x16x32_bf16 v[82:85], v[164:167], v[190:193], v[82:85]
	v_mfma_f32_16x16x32_bf16 v[70:73], v[156:159], v[198:201], v[70:73]
	v_mfma_f32_16x16x32_bf16 v[66:69], v[164:167], v[198:201], v[66:69]
	s_setprio 0
	s_barrier
; #define PG8_STAGE(bufoff, gbase, voff) do { _Pragma("unroll") for (int _i = 0; _i < 2; ++_i) \
;         __builtin_amdgcn_global_load_lds((const unsigned*)((const char*)(gbase) + (voff)[_i]), (PG8_LAS unsigned*)(lds + (bufoff) + ldsw + _i * 8192), 16, 0, 0); } while (0)
; #define PG8_LDA(dst, b, h) do { _Pragma("unroll") for (int m = 0; m < 4; ++m) _Pragma("unroll") for (int k = 0; k < 2; ++k) dst[m][k] = *(const PG8_LAS bf16x8*)(lds + PG8_SA(b, h) + aoff + m * 2048 + k * 1024); } while (0)
; #define PG8_MMA(ai, bj, At, Bt) do { __builtin_amdgcn_s_setprio(1); _Pragma("unroll") for (int m = 0; m < 4; ++m) _Pragma("unroll") for (int n = 0; n < 2; ++n) _Pragma("unroll") for (int k = 0; k < 2; ++k) \
;         acc[ai][bj][m][n] = __builtin_amdgcn_mfma_f32_16x16x32_bf16(Bt[n][k], At[m][k], acc[ai][bj][m][n], 0, 0, 0); __builtin_amdgcn_s_setprio(0); } while (0)
; #define PG8_WAIT_V(n) asm volatile("s_waitcnt vmcnt(" #n ")" ::: "memory")
; #define PG8_WAIT_L(n) asm volatile("s_waitcnt lgkmcnt(" #n ")" ::: "memory")
; #define PG8_BAR __builtin_amdgcn_s_barrier()
; #define PG8_SCHED __builtin_amdgcn_sched_barrier(0)
; template <class Epi, class Sched, bool ALIGN_EPI = false, bool SP2 = false, bool GATHER = false>
; __device__ __forceinline__ void gemm_phase(PG8_LAS unsigned char* lds, const Gemm g, const Sched& S, const Epi& E, const int2* gslot = nullptr, PG8_LAS unsigned char* gtab = nullptr) {
;     ...
;             PG8_LDA(At, 1, 1); PG8_STAGE(PG8_SB(1, 0), b3, voffB); PG8_STAGE(PG8_SB(1, 1), b3 + hstep, voffB); PG8_STAGE(PG8_SA(1, 0), a3, PG8_VA(vS, 0));
;             PG8_WAIT_V(8); PG8_WAIT_L(0); PG8_BAR; PG8_MMA(1, 0, At, B0); PG8_MMA(1, 1, At, B1); PG8_BAR; PG8_SCHED;
;     ...
;         if constexpr (ALIGN_EPI) { if (wr == 0) PG8_BAR; }
	s_add_i32 s2, s2, s45
	v_lshl_add_u64 v[202:203], v[202:203], 0, s[54:55]
	s_mov_b32 m0, s2
	ds_read_b128 v[168:171], v181 offset:49152
	ds_read_b128 v[172:175], v181 offset:50176
	ds_read_b128 v[176:179], v181 offset:51200
	ds_read_b128 v[182:185], v181 offset:52224
	ds_read_b128 v[186:189], v181 offset:53248
	ds_read_b128 v[190:193], v181 offset:54272
	ds_read_b128 v[194:197], v181 offset:55296
	ds_read_b128 v[198:201], v181 offset:56320
	global_load_lds_dwordx4 v[202:203], off
	s_add_i32 m0, s2, 0x2000
	s_add_u32 s30, s36, 0x80080
	v_lshl_add_u64 v[202:203], v[204:205], 0, s[54:55]
	s_addc_u32 s31, s37, 0
	s_add_i32 s2, s67, s45
	global_load_lds_dwordx4 v[202:203], off
	v_lshl_add_u64 v[202:203], s[30:31], 0, v[0:1]
	s_mov_b32 m0, s2
	s_nop 0
	global_load_lds_dwordx4 v[202:203], off
	v_lshl_add_u64 v[202:203], s[30:31], 0, v[130:131]
	s_add_i32 m0, s2, 0x2000
	s_nop 0
	global_load_lds_dwordx4 v[202:203], off
	v_lshl_add_u64 v[202:203], v[206:207], 0, s[54:55]
	s_mov_b32 m0, s52
	s_nop 0
	global_load_lds_dwordx4 v[202:203], off
	v_lshl_add_u64 v[202:203], v[208:209], 0, s[54:55]
	s_mov_b32 m0, s53
	s_nop 0
	global_load_lds_dwordx4 v[202:203], off
	s_waitcnt vmcnt(8)
	s_waitcnt lgkmcnt(0)
	s_barrier
	s_setprio 1
	v_mfma_f32_16x16x32_bf16 v[62:65], v[136:139], v[168:171], v[62:65]
	v_mfma_f32_16x16x32_bf16 v[58:61], v[144:147], v[168:171], v[58:61]
	v_mfma_f32_16x16x32_bf16 v[46:49], v[136:139], v[176:179], v[46:49]
	v_mfma_f32_16x16x32_bf16 v[42:45], v[144:147], v[176:179], v[42:45]
	v_mfma_f32_16x16x32_bf16 v[30:33], v[136:139], v[186:189], v[30:33]
	v_mfma_f32_16x16x32_bf16 v[26:29], v[144:147], v[186:189], v[26:29]
	v_mfma_f32_16x16x32_bf16 v[14:17], v[136:139], v[194:197], v[14:17]
	v_mfma_f32_16x16x32_bf16 v[10:13], v[144:147], v[194:197], v[10:13]
	v_mfma_f32_16x16x32_bf16 v[62:65], v[140:143], v[172:175], v[62:65]
	v_mfma_f32_16x16x32_bf16 v[58:61], v[148:151], v[172:175], v[58:61]
	v_mfma_f32_16x16x32_bf16 v[46:49], v[140:143], v[182:185], v[46:49]
	v_mfma_f32_16x16x32_bf16 v[42:45], v[148:151], v[182:185], v[42:45]
	v_mfma_f32_16x16x32_bf16 v[30:33], v[140:143], v[190:193], v[30:33]
	v_mfma_f32_16x16x32_bf16 v[26:29], v[148:151], v[190:193], v[26:29]
	v_mfma_f32_16x16x32_bf16 v[14:17], v[140:143], v[198:201], v[14:17]
	v_mfma_f32_16x16x32_bf16 v[10:13], v[148:151], v[198:201], v[10:13]
	v_mfma_f32_16x16x32_bf16 v[54:57], v[152:155], v[168:171], v[54:57]
	v_mfma_f32_16x16x32_bf16 v[50:53], v[160:163], v[168:171], v[50:53]
	v_mfma_f32_16x16x32_bf16 v[38:41], v[152:155], v[176:179], v[38:41]
	v_mfma_f32_16x16x32_bf16 v[34:37], v[160:163], v[176:179], v[34:37]
	v_mfma_f32_16x16x32_bf16 v[22:25], v[152:155], v[186:189], v[22:25]
	v_mfma_f32_16x16x32_bf16 v[18:21], v[160:163], v[186:189], v[18:21]
	v_mfma_f32_16x16x32_bf16 v[6:9], v[152:155], v[194:197], v[6:9]
	v_mfma_f32_16x16x32_bf16 v[2:5], v[160:163], v[194:197], v[2:5]
	v_mfma_f32_16x16x32_bf16 v[54:57], v[156:159], v[172:175], v[54:57]
	v_mfma_f32_16x16x32_bf16 v[50:53], v[164:167], v[172:175], v[50:53]
	v_mfma_f32_16x16x32_bf16 v[38:41], v[156:159], v[182:185], v[38:41]
	v_mfma_f32_16x16x32_bf16 v[34:37], v[164:167], v[182:185], v[34:37]
	v_mfma_f32_16x16x32_bf16 v[22:25], v[156:159], v[190:193], v[22:25]
	v_mfma_f32_16x16x32_bf16 v[18:21], v[164:167], v[190:193], v[18:21]
	v_mfma_f32_16x16x32_bf16 v[6:9], v[156:159], v[198:201], v[6:9]
	v_mfma_f32_16x16x32_bf16 v[2:5], v[164:167], v[198:201], v[2:5]
	s_setprio 0
	s_barrier
	s_add_i32 s66, s66, 2
	s_add_u32 s64, s64, 0x100
	s_addc_u32 s65, s65, 0
	s_cmp_gt_u32 s66, 29
	s_mov_b64 s[30:31], s[34:35]
	s_cbranch_scc0 .LBB0_482
	s_and_b64 vcc, exec, s[20:21]
	s_cbranch_vccz .LBB0_485
	s_barrier

; #define PG8_GREAD(dst, u, par) do { _Pragma("unroll") for (int h_ = 0; h_ < 2; ++h_) _Pragma("unroll") for (int i_ = 0; i_ < 2; ++i_) { const int rl_ = 128 * h_ + grl[i_]; \
;         const int tk_ = *(const PG8_LAS int*)(gtab + (par) * 2048 + rl_ * 8); const unsigned tok_ = (rl_ < (u).rows) ? ((unsigned)tk_ >> 2) : 0u; dst[h_][i_] = tok_ * (unsigned)(K * 2) + gcb[i_]; } } while (0)
; #define PG8_STAGE(bufoff, gbase, voff) do { _Pragma("unroll") for (int _i = 0; _i < 2; ++_i) \
;         __builtin_amdgcn_global_load_lds((const unsigned*)((const char*)(gbase) + (voff)[_i]), (PG8_LAS unsigned*)(lds + (bufoff) + ldsw + _i * 8192), 16, 0, 0); } while (0)
; #define PG8_WAIT_V(n) asm volatile("s_waitcnt vmcnt(" #n ")" ::: "memory")
; template <class Epi, class Sched, bool ALIGN_EPI = false, bool SP2 = false, bool GATHER = false>
; __device__ __forceinline__ void gemm_phase(PG8_LAS unsigned char* lds, const Gemm g, const Sched& S, const Epi& E, const int2* gslot = nullptr, PG8_LAS unsigned char* gtab = nullptr) {
;     ...
;             const char* a1 = cA + (size_t)(t + 1) * kstep;
;             const char* a2 = last ? nA : cA + (size_t)(t + 2) * kstep; const char* b2 = last ? nB : cB + (size_t)(t + 2) * kstep;
;             const char* a3 = a2 + kstep; const char* b3 = b2 + kstep;
;             if (last && has_next) S.a_ready(nxt);
;             if constexpr (GATHER) { if (last) { if (has_next) { PG8_GREAD(vN, nxt, (ui + 1) & 1); } else { _Pragma("unroll") for (int h_ = 0; h_ < 2; ++h_) _Pragma("unroll") for (int i_ = 0; i_ < 2; ++i_) vN[h_][i_] = vC[h_][i_]; } } }
;             unsigned vS[2][2];
; #pragma unroll
;             for (int h_ = 0; h_ < 2; ++h_)
; #pragma unroll
;                 for (int i_ = 0; i_ < 2; ++i_) vS[h_][i_] = (GATHER && last) ? vN[h_][i_] : vC[h_][i_];
;             if constexpr (SP2) {
;             PG8_LDB(B0, 0, 0); PG8_LDB(B1, 0, 1); PG8_SCHED; PG8_LDA(At, 0, 0); PG8_STAGE(PG8_SA(1, 1), a1 + PG8_AH(1), PG8_VA(vC, 1));
;             PG8_WAIT_V(8); PG8_WAIT_L(0); PG8_BAR; PG8_MMA(0, 0, At, B0); PG8_MMA(0, 1, At, B1); PG8_BAR; PG8_SCHED;
;             PG8_LDA(At, 0, 1); PG8_STAGE(PG8_SB(0, 0), b2, voffB); PG8_STAGE(PG8_SB(0, 1), b2 + hstep, voffB); PG8_STAGE(PG8_SA(0, 0), a2, PG8_VA(vS, 0));
;             PG8_WAIT_V(8); PG8_WAIT_L(0); PG8_BAR; PG8_MMA(1, 0, At, B0); PG8_MMA(1, 1, At, B1); PG8_BAR; PG8_SCHED;
.LBB0_565:
	s_add_u32 s2, s24, 0xfffc0080
	s_addc_u32 s26, s25, -1
	s_cmp_eq_u32 s62, 12
	s_cselect_b32 s29, s19, s26
	s_cselect_b32 s28, s53, s2
	s_cselect_b32 s27, s15, s61
	s_cselect_b32 s26, s56, s60
	s_add_i32 s2, 0, 0x10000
	v_add_u32_e32 v140, s2, v146
	s_add_i32 s63, 0, 0x14000
	ds_read_b128 v[142:145], v140
	ds_read_b128 v[150:153], v140 offset:1024
	ds_read_b128 v[154:157], v140 offset:2048
	ds_read_b128 v[158:161], v140 offset:3072
	v_add_u32_e32 v140, s63, v146
	ds_read_b128 v[162:165], v140
	ds_read_b128 v[166:169], v140 offset:1024
	ds_read_b128 v[170:173], v140 offset:2048
	ds_read_b128 v[174:177], v140 offset:3072
	v_lshl_add_u64 v[210:211], s[24:25], 0, v[136:137]
	s_add_i32 m0, s36, 0xc000
	ds_read_b128 v[178:181], v148
	ds_read_b128 v[182:185], v148 offset:1024
	ds_read_b128 v[186:189], v148 offset:2048
	ds_read_b128 v[190:193], v148 offset:3072
	ds_read_b128 v[194:197], v148 offset:4096
	ds_read_b128 v[198:201], v148 offset:5120
	ds_read_b128 v[202:205], v148 offset:6144
	ds_read_b128 v[206:209], v148 offset:7168
	global_load_lds_dwordx4 v[210:211], off
	v_lshl_add_u64 v[210:211], s[24:25], 0, v[138:139]
	s_add_i32 m0, s36, 0xe000
	s_nop 0
	global_load_lds_dwordx4 v[210:211], off
	s_waitcnt vmcnt(8)
	s_waitcnt lgkmcnt(0)
	s_barrier
	s_setprio 1
	v_mfma_f32_16x16x32_bf16 v[126:129], v[142:145], v[178:181], v[126:129]
	v_mfma_f32_16x16x32_bf16 v[122:125], v[154:157], v[178:181], v[122:125]
	v_mfma_f32_16x16x32_bf16 v[114:117], v[142:145], v[186:189], v[114:117]
	v_mfma_f32_16x16x32_bf16 v[106:109], v[154:157], v[186:189], v[106:109]
	v_mfma_f32_16x16x32_bf16 v[98:101], v[142:145], v[194:197], v[98:101]
	v_mfma_f32_16x16x32_bf16 v[90:93], v[154:157], v[194:197], v[90:93]
	v_mfma_f32_16x16x32_bf16 v[82:85], v[142:145], v[202:205], v[82:85]
	v_mfma_f32_16x16x32_bf16 v[74:77], v[154:157], v[202:205], v[74:77]
	v_mfma_f32_16x16x32_bf16 v[126:129], v[150:153], v[182:185], v[126:129]
	v_mfma_f32_16x16x32_bf16 v[122:125], v[158:161], v[182:185], v[122:125]
	v_mfma_f32_16x16x32_bf16 v[114:117], v[150:153], v[190:193], v[114:117]
	v_mfma_f32_16x16x32_bf16 v[106:109], v[158:161], v[190:193], v[106:109]
	v_mfma_f32_16x16x32_bf16 v[98:101], v[150:153], v[198:201], v[98:101]
	v_mfma_f32_16x16x32_bf16 v[90:93], v[158:161], v[198:201], v[90:93]
	v_mfma_f32_16x16x32_bf16 v[82:85], v[150:153], v[206:209], v[82:85]
	v_mfma_f32_16x16x32_bf16 v[74:77], v[158:161], v[206:209], v[74:77]
	v_mfma_f32_16x16x32_bf16 v[118:121], v[162:165], v[178:181], v[118:121]
	v_mfma_f32_16x16x32_bf16 v[110:113], v[170:173], v[178:181], v[110:113]
	v_mfma_f32_16x16x32_bf16 v[102:105], v[162:165], v[186:189], v[102:105]
	v_mfma_f32_16x16x32_bf16 v[94:97], v[170:173], v[186:189], v[94:97]
	v_mfma_f32_16x16x32_bf16 v[86:89], v[162:165], v[194:197], v[86:89]
	v_mfma_f32_16x16x32_bf16 v[78:81], v[170:173], v[194:197], v[78:81]
	v_mfma_f32_16x16x32_bf16 v[70:73], v[162:165], v[202:205], v[70:73]
	v_mfma_f32_16x16x32_bf16 v[66:69], v[170:173], v[202:205], v[66:69]
	v_mfma_f32_16x16x32_bf16 v[118:121], v[166:169], v[182:185], v[118:121]
	v_mfma_f32_16x16x32_bf16 v[110:113], v[174:177], v[182:185], v[110:113]
	v_mfma_f32_16x16x32_bf16 v[102:105], v[166:169], v[190:193], v[102:105]
	v_mfma_f32_16x16x32_bf16 v[94:97], v[174:177], v[190:193], v[94:97]
	v_mfma_f32_16x16x32_bf16 v[86:89], v[166:169], v[198:201], v[86:89]
	v_mfma_f32_16x16x32_bf16 v[78:81], v[174:177], v[198:201], v[78:81]
	v_mfma_f32_16x16x32_bf16 v[70:73], v[166:169], v[206:209], v[70:73]
	v_mfma_f32_16x16x32_bf16 v[66:69], v[174:177], v[206:209], v[66:69]
	s_setprio 0
	s_barrier
	s_add_i32 s2, s2, s35
	v_lshl_add_u64 v[210:211], s[26:27], 0, v[0:1]
	s_mov_b32 m0, s2
	ds_read_b128 v[178:181], v148 offset:16384
	ds_read_b128 v[182:185], v148 offset:17408
	ds_read_b128 v[186:189], v148 offset:18432
	ds_read_b128 v[190:193], v148 offset:19456
	ds_read_b128 v[194:197], v148 offset:20480
	ds_read_b128 v[198:201], v148 offset:21504
	ds_read_b128 v[202:205], v148 offset:22528
	ds_read_b128 v[206:209], v148 offset:23552
	global_load_lds_dwordx4 v[210:211], off
	s_add_i32 m0, s2, 0x2000
	s_add_u32 s64, s26, 0x40000
	v_lshl_add_u64 v[212:213], s[26:27], 0, v[130:131]
	s_addc_u32 s65, s27, 0
	s_add_i32 s2, s63, s35
	global_load_lds_dwordx4 v[212:213], off
	v_lshl_add_u64 v[214:215], s[64:65], 0, v[0:1]
	s_mov_b32 m0, s2
	v_lshl_add_u64 v[216:217], s[28:29], 0, v[132:133]
	global_load_lds_dwordx4 v[214:215], off
	v_lshl_add_u64 v[214:215], s[64:65], 0, v[130:131]
	s_add_i32 m0, s2, 0x2000
	s_nop 0
	global_load_lds_dwordx4 v[214:215], off
	v_lshl_add_u64 v[214:215], s[28:29], 0, v[134:135]
	s_mov_b32 m0, s36
	s_nop 0
	global_load_lds_dwordx4 v[214:215], off
	s_mov_b32 m0, s37
	s_nop 0
	global_load_lds_dwordx4 v[216:217], off
	s_waitcnt vmcnt(8)
	s_waitcnt lgkmcnt(0)
	s_barrier
; #define PG8_STAGE(bufoff, gbase, voff) do { _Pragma("unroll") for (int _i = 0; _i < 2; ++_i) \
;         __builtin_amdgcn_global_load_lds((const unsigned*)((const char*)(gbase) + (voff)[_i]), (PG8_LAS unsigned*)(lds + (bufoff) + ldsw + _i * 8192), 16, 0, 0); } while (0)
; #define PG8_LDA(dst, b, h) do { _Pragma("unroll") for (int m = 0; m < 4; ++m) _Pragma("unroll") for (int k = 0; k < 2; ++k) dst[m][k] = *(const PG8_LAS bf16x8*)(lds + PG8_SA(b, h) + aoff + m * 2048 + k * 1024); } while (0)
; #define PG8_LDB(dst, b, h) do { _Pragma("unroll") for (int n = 0; n < 2; ++n) _Pragma("unroll") for (int k = 0; k < 2; ++k) dst[n][k] = *(const PG8_LAS bf16x8*)(lds + PG8_SB(b, h) + boff + n * 2048 + k * 1024); } while (0)
; #define PG8_MMA(ai, bj, At, Bt) do { __builtin_amdgcn_s_setprio(1); _Pragma("unroll") for (int m = 0; m < 4; ++m) _Pragma("unroll") for (int n = 0; n < 2; ++n) _Pragma("unroll") for (int k = 0; k < 2; ++k) \
;         acc[ai][bj][m][n] = __builtin_amdgcn_mfma_f32_16x16x32_bf16(Bt[n][k], At[m][k], acc[ai][bj][m][n], 0, 0, 0); __builtin_amdgcn_s_setprio(0); } while (0)
; #define PG8_WAIT_V(n) asm volatile("s_waitcnt vmcnt(" #n ")" ::: "memory")
; #define PG8_WAIT_L(n) asm volatile("s_waitcnt lgkmcnt(" #n ")" ::: "memory")
; #define PG8_BAR __builtin_amdgcn_s_barrier()
; #define PG8_SCHED __builtin_amdgcn_sched_barrier(0)
; template <class Epi, class Sched, bool ALIGN_EPI = false, bool SP2 = false, bool GATHER = false>
; __device__ __forceinline__ void gemm_phase(PG8_LAS unsigned char* lds, const Gemm g, const Sched& S, const Epi& E, const int2* gslot = nullptr, PG8_LAS unsigned char* gtab = nullptr) {
;     ...
;             PG8_WAIT_V(8); PG8_WAIT_L(0); PG8_BAR; PG8_MMA(1, 0, At, B0); PG8_MMA(1, 1, At, B1); PG8_BAR; PG8_SCHED;
;             PG8_LDB(B0, 1, 0); PG8_LDB(B1, 1, 1); PG8_SCHED; PG8_LDA(At, 1, 0); PG8_STAGE(PG8_SA(0, 1), a2 + PG8_AH(1), PG8_VA(vS, 1));
;             PG8_WAIT_V(8); PG8_WAIT_L(0); PG8_BAR; PG8_MMA(0, 0, At, B0); PG8_MMA(0, 1, At, B1); PG8_BAR; PG8_SCHED;
	s_setprio 1
	v_mfma_f32_16x16x32_bf16 v[62:65], v[142:145], v[178:181], v[62:65]
	v_mfma_f32_16x16x32_bf16 v[58:61], v[154:157], v[178:181], v[58:61]
	v_mfma_f32_16x16x32_bf16 v[50:53], v[142:145], v[186:189], v[50:53]
	v_mfma_f32_16x16x32_bf16 v[42:45], v[154:157], v[186:189], v[42:45]
	v_mfma_f32_16x16x32_bf16 v[34:37], v[142:145], v[194:197], v[34:37]
	v_mfma_f32_16x16x32_bf16 v[26:29], v[154:157], v[194:197], v[26:29]
	v_mfma_f32_16x16x32_bf16 v[18:21], v[142:145], v[202:205], v[18:21]
	v_mfma_f32_16x16x32_bf16 v[10:13], v[154:157], v[202:205], v[10:13]
	v_mfma_f32_16x16x32_bf16 v[62:65], v[150:153], v[182:185], v[62:65]
	v_mfma_f32_16x16x32_bf16 v[58:61], v[158:161], v[182:185], v[58:61]
	v_mfma_f32_16x16x32_bf16 v[50:53], v[150:153], v[190:193], v[50:53]
	v_mfma_f32_16x16x32_bf16 v[42:45], v[158:161], v[190:193], v[42:45]
	v_mfma_f32_16x16x32_bf16 v[34:37], v[150:153], v[198:201], v[34:37]
	v_mfma_f32_16x16x32_bf16 v[26:29], v[158:161], v[198:201], v[26:29]
	v_mfma_f32_16x16x32_bf16 v[18:21], v[150:153], v[206:209], v[18:21]
	v_mfma_f32_16x16x32_bf16 v[10:13], v[158:161], v[206:209], v[10:13]
	v_mfma_f32_16x16x32_bf16 v[54:57], v[162:165], v[178:181], v[54:57]
	v_mfma_f32_16x16x32_bf16 v[46:49], v[170:173], v[178:181], v[46:49]
	v_mfma_f32_16x16x32_bf16 v[38:41], v[162:165], v[186:189], v[38:41]
	v_mfma_f32_16x16x32_bf16 v[30:33], v[170:173], v[186:189], v[30:33]
	v_mfma_f32_16x16x32_bf16 v[22:25], v[162:165], v[194:197], v[22:25]
	v_mfma_f32_16x16x32_bf16 v[14:17], v[170:173], v[194:197], v[14:17]
	v_mfma_f32_16x16x32_bf16 v[6:9], v[162:165], v[202:205], v[6:9]
	v_mfma_f32_16x16x32_bf16 v[2:5], v[170:173], v[202:205], v[2:5]
	v_mfma_f32_16x16x32_bf16 v[54:57], v[166:169], v[182:185], v[54:57]
	v_mfma_f32_16x16x32_bf16 v[46:49], v[174:177], v[182:185], v[46:49]
	v_mfma_f32_16x16x32_bf16 v[38:41], v[166:169], v[190:193], v[38:41]
	v_mfma_f32_16x16x32_bf16 v[30:33], v[174:177], v[190:193], v[30:33]
	v_mfma_f32_16x16x32_bf16 v[22:25], v[166:169], v[198:201], v[22:25]
	v_mfma_f32_16x16x32_bf16 v[14:17], v[174:177], v[198:201], v[14:17]
	v_mfma_f32_16x16x32_bf16 v[6:9], v[166:169], v[206:209], v[6:9]
	v_mfma_f32_16x16x32_bf16 v[2:5], v[174:177], v[206:209], v[2:5]
	s_setprio 0
	s_barrier
	s_add_i32 s2, 0, 0x18000
	v_add_u32_e32 v140, s2, v146
	s_add_i32 s63, 0, 0x1c000
	ds_read_b128 v[142:145], v140
	ds_read_b128 v[150:153], v140 offset:1024
	ds_read_b128 v[154:157], v140 offset:2048
	ds_read_b128 v[158:161], v140 offset:3072
	v_add_u32_e32 v140, s63, v146
	ds_read_b128 v[162:165], v140
	ds_read_b128 v[166:169], v140 offset:1024
	ds_read_b128 v[170:173], v140 offset:2048
	ds_read_b128 v[174:177], v140 offset:3072
	s_add_u32 s28, s28, 0x40000
	s_addc_u32 s29, s29, 0
	s_mov_b32 m0, s38
	v_lshl_add_u64 v[218:219], s[28:29], 0, v[134:135]
	ds_read_b128 v[178:181], v148 offset:32768
	ds_read_b128 v[182:185], v148 offset:33792
	ds_read_b128 v[186:189], v148 offset:34816
	ds_read_b128 v[190:193], v148 offset:35840
	ds_read_b128 v[194:197], v148 offset:36864
	ds_read_b128 v[198:201], v148 offset:37888
	ds_read_b128 v[202:205], v148 offset:38912
	ds_read_b128 v[206:209], v148 offset:39936
	global_load_lds_dwordx4 v[218:219], off
	v_lshl_add_u64 v[218:219], s[28:29], 0, v[132:133]
	s_mov_b32 m0, s39
	s_nop 0
	global_load_lds_dwordx4 v[218:219], off
	s_waitcnt vmcnt(8)
	s_waitcnt lgkmcnt(0)
	s_barrier
	s_setprio 1
	v_mfma_f32_16x16x32_bf16 v[126:129], v[142:145], v[178:181], v[126:129]
	v_mfma_f32_16x16x32_bf16 v[122:125], v[154:157], v[178:181], v[122:125]
	v_mfma_f32_16x16x32_bf16 v[114:117], v[142:145], v[186:189], v[114:117]
	v_mfma_f32_16x16x32_bf16 v[106:109], v[154:157], v[186:189], v[106:109]
	v_mfma_f32_16x16x32_bf16 v[98:101], v[142:145], v[194:197], v[98:101]
	v_mfma_f32_16x16x32_bf16 v[90:93], v[154:157], v[194:197], v[90:93]
	v_mfma_f32_16x16x32_bf16 v[82:85], v[142:145], v[202:205], v[82:85]
	v_mfma_f32_16x16x32_bf16 v[74:77], v[154:157], v[202:205], v[74:77]
	v_mfma_f32_16x16x32_bf16 v[126:129], v[150:153], v[182:185], v[126:129]
	v_mfma_f32_16x16x32_bf16 v[122:125], v[158:161], v[182:185], v[122:125]
	v_mfma_f32_16x16x32_bf16 v[114:117], v[150:153], v[190:193], v[114:117]
	v_mfma_f32_16x16x32_bf16 v[106:109], v[158:161], v[190:193], v[106:109]
	v_mfma_f32_16x16x32_bf16 v[98:101], v[150:153], v[198:201], v[98:101]
	v_mfma_f32_16x16x32_bf16 v[90:93], v[158:161], v[198:201], v[90:93]
	v_mfma_f32_16x16x32_bf16 v[82:85], v[150:153], v[206:209], v[82:85]
	v_mfma_f32_16x16x32_bf16 v[74:77], v[158:161], v[206:209], v[74:77]
	v_mfma_f32_16x16x32_bf16 v[118:121], v[162:165], v[178:181], v[118:121]
	v_mfma_f32_16x16x32_bf16 v[110:113], v[170:173], v[178:181], v[110:113]
	v_mfma_f32_16x16x32_bf16 v[102:105], v[162:165], v[186:189], v[102:105]
	v_mfma_f32_16x16x32_bf16 v[94:97], v[170:173], v[186:189], v[94:97]
	v_mfma_f32_16x16x32_bf16 v[86:89], v[162:165], v[194:197], v[86:89]
	v_mfma_f32_16x16x32_bf16 v[78:81], v[170:173], v[194:197], v[78:81]
	v_mfma_f32_16x16x32_bf16 v[70:73], v[162:165], v[202:205], v[70:73]
	v_mfma_f32_16x16x32_bf16 v[66:69], v[170:173], v[202:205], v[66:69]
	v_mfma_f32_16x16x32_bf16 v[118:121], v[166:169], v[182:185], v[118:121]
	v_mfma_f32_16x16x32_bf16 v[110:113], v[174:177], v[182:185], v[110:113]
	v_mfma_f32_16x16x32_bf16 v[102:105], v[166:169], v[190:193], v[102:105]
	v_mfma_f32_16x16x32_bf16 v[94:97], v[174:177], v[190:193], v[94:97]
	v_mfma_f32_16x16x32_bf16 v[86:89], v[166:169], v[198:201], v[86:89]
	v_mfma_f32_16x16x32_bf16 v[78:81], v[174:177], v[198:201], v[78:81]
	v_mfma_f32_16x16x32_bf16 v[70:73], v[166:169], v[206:209], v[70:73]
	v_mfma_f32_16x16x32_bf16 v[66:69], v[174:177], v[206:209], v[66:69]
	s_setprio 0
	s_barrier
; #define PG8_STAGE(bufoff, gbase, voff) do { _Pragma("unroll") for (int _i = 0; _i < 2; ++_i) \
;         __builtin_amdgcn_global_load_lds((const unsigned*)((const char*)(gbase) + (voff)[_i]), (PG8_LAS unsigned*)(lds + (bufoff) + ldsw + _i * 8192), 16, 0, 0); } while (0)
; #define PG8_LDA(dst, b, h) do { _Pragma("unroll") for (int m = 0; m < 4; ++m) _Pragma("unroll") for (int k = 0; k < 2; ++k) dst[m][k] = *(const PG8_LAS bf16x8*)(lds + PG8_SA(b, h) + aoff + m * 2048 + k * 1024); } while (0)
; #define PG8_MMA(ai, bj, At, Bt) do { __builtin_amdgcn_s_setprio(1); _Pragma("unroll") for (int m = 0; m < 4; ++m) _Pragma("unroll") for (int n = 0; n < 2; ++n) _Pragma("unroll") for (int k = 0; k < 2; ++k) \
;         acc[ai][bj][m][n] = __builtin_amdgcn_mfma_f32_16x16x32_bf16(Bt[n][k], At[m][k], acc[ai][bj][m][n], 0, 0, 0); __builtin_amdgcn_s_setprio(0); } while (0)
; #define PG8_WAIT_V(n) asm volatile("s_waitcnt vmcnt(" #n ")" ::: "memory")
; #define PG8_WAIT_L(n) asm volatile("s_waitcnt lgkmcnt(" #n ")" ::: "memory")
; #define PG8_BAR __builtin_amdgcn_s_barrier()
; #define PG8_SCHED __builtin_amdgcn_sched_barrier(0)
; template <class Epi, class Sched, bool ALIGN_EPI = false, bool SP2 = false, bool GATHER = false>
; __device__ __forceinline__ void gemm_phase(PG8_LAS unsigned char* lds, const Gemm g, const Sched& S, const Epi& E, const int2* gslot = nullptr, PG8_LAS unsigned char* gtab = nullptr) {
;     ...
;             PG8_LDA(At, 1, 1); PG8_STAGE(PG8_SB(1, 0), b3, voffB); PG8_STAGE(PG8_SB(1, 1), b3 + hstep, voffB); PG8_STAGE(PG8_SA(1, 0), a3, PG8_VA(vS, 0));
;             PG8_WAIT_V(8); PG8_WAIT_L(0); PG8_BAR; PG8_MMA(1, 0, At, B0); PG8_MMA(1, 1, At, B1); PG8_BAR; PG8_SCHED;
;     ...
;         if constexpr (ALIGN_EPI) { if (wr == 0) PG8_BAR; }
	s_add_i32 s2, s2, s35
	v_lshl_add_u64 v[210:211], v[210:211], 0, s[54:55]
	s_mov_b32 m0, s2
	ds_read_b128 v[178:181], v148 offset:49152
	ds_read_b128 v[182:185], v148 offset:50176
	ds_read_b128 v[186:189], v148 offset:51200
	ds_read_b128 v[190:193], v148 offset:52224
	ds_read_b128 v[194:197], v148 offset:53248
	ds_read_b128 v[198:201], v148 offset:54272
	ds_read_b128 v[202:205], v148 offset:55296
	ds_read_b128 v[206:209], v148 offset:56320
	global_load_lds_dwordx4 v[210:211], off
	s_add_i32 m0, s2, 0x2000
	s_add_u32 s26, s26, 0x40080
	v_lshl_add_u64 v[210:211], v[212:213], 0, s[54:55]
	s_addc_u32 s27, s27, 0
	s_add_i32 s2, s63, s35
	global_load_lds_dwordx4 v[210:211], off
	v_lshl_add_u64 v[210:211], s[26:27], 0, v[0:1]
	s_mov_b32 m0, s2
	s_nop 0
	global_load_lds_dwordx4 v[210:211], off
	v_lshl_add_u64 v[210:211], s[26:27], 0, v[130:131]
	s_add_i32 m0, s2, 0x2000
	s_nop 0
	global_load_lds_dwordx4 v[210:211], off
	v_lshl_add_u64 v[210:211], v[214:215], 0, s[54:55]
	s_mov_b32 m0, s44
	s_nop 0
	global_load_lds_dwordx4 v[210:211], off
	v_lshl_add_u64 v[210:211], v[216:217], 0, s[54:55]
	s_mov_b32 m0, s45
	s_nop 0
	global_load_lds_dwordx4 v[210:211], off
	s_waitcnt vmcnt(8)
	s_waitcnt lgkmcnt(0)
	s_barrier
	s_setprio 1
	v_mfma_f32_16x16x32_bf16 v[62:65], v[142:145], v[178:181], v[62:65]
	v_mfma_f32_16x16x32_bf16 v[58:61], v[154:157], v[178:181], v[58:61]
	v_mfma_f32_16x16x32_bf16 v[50:53], v[142:145], v[186:189], v[50:53]
	v_mfma_f32_16x16x32_bf16 v[42:45], v[154:157], v[186:189], v[42:45]
	v_mfma_f32_16x16x32_bf16 v[34:37], v[142:145], v[194:197], v[34:37]
	v_mfma_f32_16x16x32_bf16 v[26:29], v[154:157], v[194:197], v[26:29]
	v_mfma_f32_16x16x32_bf16 v[18:21], v[142:145], v[202:205], v[18:21]
	v_mfma_f32_16x16x32_bf16 v[10:13], v[154:157], v[202:205], v[10:13]
	v_mfma_f32_16x16x32_bf16 v[62:65], v[150:153], v[182:185], v[62:65]
	v_mfma_f32_16x16x32_bf16 v[58:61], v[158:161], v[182:185], v[58:61]
	v_mfma_f32_16x16x32_bf16 v[50:53], v[150:153], v[190:193], v[50:53]
	v_mfma_f32_16x16x32_bf16 v[42:45], v[158:161], v[190:193], v[42:45]
	v_mfma_f32_16x16x32_bf16 v[34:37], v[150:153], v[198:201], v[34:37]
	v_mfma_f32_16x16x32_bf16 v[26:29], v[158:161], v[198:201], v[26:29]
	v_mfma_f32_16x16x32_bf16 v[18:21], v[150:153], v[206:209], v[18:21]
	v_mfma_f32_16x16x32_bf16 v[10:13], v[158:161], v[206:209], v[10:13]
	v_mfma_f32_16x16x32_bf16 v[54:57], v[162:165], v[178:181], v[54:57]
	v_mfma_f32_16x16x32_bf16 v[46:49], v[170:173], v[178:181], v[46:49]
	v_mfma_f32_16x16x32_bf16 v[38:41], v[162:165], v[186:189], v[38:41]
	v_mfma_f32_16x16x32_bf16 v[30:33], v[170:173], v[186:189], v[30:33]
	v_mfma_f32_16x16x32_bf16 v[22:25], v[162:165], v[194:197], v[22:25]
	v_mfma_f32_16x16x32_bf16 v[14:17], v[170:173], v[194:197], v[14:17]
	v_mfma_f32_16x16x32_bf16 v[6:9], v[162:165], v[202:205], v[6:9]
	v_mfma_f32_16x16x32_bf16 v[2:5], v[170:173], v[202:205], v[2:5]
	v_mfma_f32_16x16x32_bf16 v[54:57], v[166:169], v[182:185], v[54:57]
	v_mfma_f32_16x16x32_bf16 v[46:49], v[174:177], v[182:185], v[46:49]
	v_mfma_f32_16x16x32_bf16 v[38:41], v[166:169], v[190:193], v[38:41]
	v_mfma_f32_16x16x32_bf16 v[30:33], v[174:177], v[190:193], v[30:33]
	v_mfma_f32_16x16x32_bf16 v[22:25], v[166:169], v[198:201], v[22:25]
	v_mfma_f32_16x16x32_bf16 v[14:17], v[174:177], v[198:201], v[14:17]
	v_mfma_f32_16x16x32_bf16 v[6:9], v[166:169], v[206:209], v[6:9]
	v_mfma_f32_16x16x32_bf16 v[2:5], v[174:177], v[206:209], v[2:5]
	s_setprio 0
	s_barrier
	s_add_i32 s62, s62, 2
	s_add_u32 s24, s24, 0x100
	s_addc_u32 s25, s25, 0
	s_add_u32 s60, s60, 0x100
	s_addc_u32 s61, s61, 0
	s_cmp_gt_u32 s62, 13
	s_cbranch_scc0 .LBB0_565
	s_and_b64 vcc, exec, s[12:13]
	s_cbranch_vccz .LBB0_568
	s_barrier

; #define PG8_GREAD(dst, u, par) do { _Pragma("unroll") for (int h_ = 0; h_ < 2; ++h_) _Pragma("unroll") for (int i_ = 0; i_ < 2; ++i_) { const int rl_ = 128 * h_ + grl[i_]; \
;         const int tk_ = *(const PG8_LAS int*)(gtab + (par) * 2048 + rl_ * 8); const unsigned tok_ = (rl_ < (u).rows) ? ((unsigned)tk_ >> 2) : 0u; dst[h_][i_] = tok_ * (unsigned)(K * 2) + gcb[i_]; } } while (0)
; #define PG8_STAGE(bufoff, gbase, voff) do { _Pragma("unroll") for (int _i = 0; _i < 2; ++_i) \
;         __builtin_amdgcn_global_load_lds((const unsigned*)((const char*)(gbase) + (voff)[_i]), (PG8_LAS unsigned*)(lds + (bufoff) + ldsw + _i * 8192), 16, 0, 0); } while (0)
; #define PG8_WAIT_V(n) asm volatile("s_waitcnt vmcnt(" #n ")" ::: "memory")
; template <class Epi, class Sched, bool ALIGN_EPI = false, bool SP2 = false, bool GATHER = false>
; __device__ __forceinline__ void gemm_phase(PG8_LAS unsigned char* lds, const Gemm g, const Sched& S, const Epi& E, const int2* gslot = nullptr, PG8_LAS unsigned char* gtab = nullptr) {
;     ...
;             const char* a1 = cA + (size_t)(t + 1) * kstep;
;             const char* a2 = last ? nA : cA + (size_t)(t + 2) * kstep; const char* b2 = last ? nB : cB + (size_t)(t + 2) * kstep;
;             const char* a3 = a2 + kstep; const char* b3 = b2 + kstep;
;             if (last && has_next) S.a_ready(nxt);
;             if constexpr (GATHER) { if (last) { if (has_next) { PG8_GREAD(vN, nxt, (ui + 1) & 1); } else { _Pragma("unroll") for (int h_ = 0; h_ < 2; ++h_) _Pragma("unroll") for (int i_ = 0; i_ < 2; ++i_) vN[h_][i_] = vC[h_][i_]; } } }
;             unsigned vS[2][2];
; #pragma unroll
;             for (int h_ = 0; h_ < 2; ++h_)
; #pragma unroll
;                 for (int i_ = 0; i_ < 2; ++i_) vS[h_][i_] = (GATHER && last) ? vN[h_][i_] : vC[h_][i_];
;             if constexpr (SP2) {
;             PG8_LDB(B0, 0, 0); PG8_LDB(B1, 0, 1); PG8_SCHED; PG8_LDA(At, 0, 0); PG8_STAGE(PG8_SA(1, 1), a1 + PG8_AH(1), PG8_VA(vC, 1));
;             PG8_WAIT_V(8); PG8_WAIT_L(0); PG8_BAR; PG8_MMA(0, 0, At, B0); PG8_MMA(0, 1, At, B1); PG8_BAR; PG8_SCHED;
;             PG8_LDA(At, 0, 1); PG8_STAGE(PG8_SB(0, 0), b2, voffB); PG8_STAGE(PG8_SB(0, 1), b2 + hstep, voffB); PG8_STAGE(PG8_SA(0, 0), a2, PG8_VA(vS, 0));
;             PG8_WAIT_V(8); PG8_WAIT_L(0); PG8_BAR; PG8_MMA(1, 0, At, B0); PG8_MMA(1, 1, At, B1); PG8_BAR; PG8_SCHED;
.LBB0_813:
	s_add_u32 s30, s28, 0x100
	s_addc_u32 s31, s29, 0
	s_cmp_eq_u32 s63, 12
	s_cselect_b32 s37, s23, s31
	s_cselect_b32 s36, s59, s30
	s_cselect_b32 s35, s21, s62
	s_cselect_b32 s34, s60, s61
	s_add_i32 s2, 0, 0x10000
	s_add_i32 s64, 0, 0x14000
	v_add_u32_e32 v148, s2, v215
	v_add_u32_e32 v164, s64, v215
	ds_read_b128 v[136:139], v148
	ds_read_b128 v[140:143], v148 offset:1024
	ds_read_b128 v[144:147], v148 offset:2048
	ds_read_b128 v[148:151], v148 offset:3072
	ds_read_b128 v[152:155], v164
	ds_read_b128 v[156:159], v164 offset:1024
	ds_read_b128 v[160:163], v164 offset:2048
	ds_read_b128 v[164:167], v164 offset:3072
	v_lshl_add_u64 v[202:203], s[28:29], 0, v[132:133]
	s_add_i32 m0, s44, 0xc000
	ds_read_b128 v[168:171], v181
	ds_read_b128 v[172:175], v181 offset:1024
	ds_read_b128 v[176:179], v181 offset:2048
	ds_read_b128 v[182:185], v181 offset:3072
	ds_read_b128 v[186:189], v181 offset:4096
	ds_read_b128 v[190:193], v181 offset:5120
	ds_read_b128 v[194:197], v181 offset:6144
	ds_read_b128 v[198:201], v181 offset:7168
	global_load_lds_dwordx4 v[202:203], off
	v_lshl_add_u64 v[202:203], s[28:29], 0, v[134:135]
	s_add_i32 m0, s44, 0xe000
	s_nop 0
	global_load_lds_dwordx4 v[202:203], off
	s_waitcnt vmcnt(8)
	s_waitcnt lgkmcnt(0)
	s_barrier
	s_setprio 1
	v_mfma_f32_16x16x32_bf16 v[126:129], v[136:139], v[168:171], v[126:129]
	v_mfma_f32_16x16x32_bf16 v[122:125], v[144:147], v[168:171], v[122:125]
	v_mfma_f32_16x16x32_bf16 v[110:113], v[136:139], v[176:179], v[110:113]
	v_mfma_f32_16x16x32_bf16 v[106:109], v[144:147], v[176:179], v[106:109]
	v_mfma_f32_16x16x32_bf16 v[94:97], v[136:139], v[186:189], v[94:97]
	v_mfma_f32_16x16x32_bf16 v[90:93], v[144:147], v[186:189], v[90:93]
	v_mfma_f32_16x16x32_bf16 v[78:81], v[136:139], v[194:197], v[78:81]
	v_mfma_f32_16x16x32_bf16 v[74:77], v[144:147], v[194:197], v[74:77]
	v_mfma_f32_16x16x32_bf16 v[126:129], v[140:143], v[172:175], v[126:129]
	v_mfma_f32_16x16x32_bf16 v[122:125], v[148:151], v[172:175], v[122:125]
	v_mfma_f32_16x16x32_bf16 v[110:113], v[140:143], v[182:185], v[110:113]
	v_mfma_f32_16x16x32_bf16 v[106:109], v[148:151], v[182:185], v[106:109]
	v_mfma_f32_16x16x32_bf16 v[94:97], v[140:143], v[190:193], v[94:97]
	v_mfma_f32_16x16x32_bf16 v[90:93], v[148:151], v[190:193], v[90:93]
	v_mfma_f32_16x16x32_bf16 v[78:81], v[140:143], v[198:201], v[78:81]
	v_mfma_f32_16x16x32_bf16 v[74:77], v[148:151], v[198:201], v[74:77]
	v_mfma_f32_16x16x32_bf16 v[118:121], v[152:155], v[168:171], v[118:121]
	v_mfma_f32_16x16x32_bf16 v[114:117], v[160:163], v[168:171], v[114:117]
	v_mfma_f32_16x16x32_bf16 v[102:105], v[152:155], v[176:179], v[102:105]
	v_mfma_f32_16x16x32_bf16 v[98:101], v[160:163], v[176:179], v[98:101]
	v_mfma_f32_16x16x32_bf16 v[86:89], v[152:155], v[186:189], v[86:89]
	v_mfma_f32_16x16x32_bf16 v[82:85], v[160:163], v[186:189], v[82:85]
	v_mfma_f32_16x16x32_bf16 v[70:73], v[152:155], v[194:197], v[70:73]
	v_mfma_f32_16x16x32_bf16 v[66:69], v[160:163], v[194:197], v[66:69]
	v_mfma_f32_16x16x32_bf16 v[118:121], v[156:159], v[172:175], v[118:121]
	v_mfma_f32_16x16x32_bf16 v[114:117], v[164:167], v[172:175], v[114:117]
	v_mfma_f32_16x16x32_bf16 v[102:105], v[156:159], v[182:185], v[102:105]
	v_mfma_f32_16x16x32_bf16 v[98:101], v[164:167], v[182:185], v[98:101]
	v_mfma_f32_16x16x32_bf16 v[86:89], v[156:159], v[190:193], v[86:89]
	v_mfma_f32_16x16x32_bf16 v[82:85], v[164:167], v[190:193], v[82:85]
	v_mfma_f32_16x16x32_bf16 v[70:73], v[156:159], v[198:201], v[70:73]
	v_mfma_f32_16x16x32_bf16 v[66:69], v[164:167], v[198:201], v[66:69]
	s_setprio 0
	s_barrier
	s_add_i32 s2, s2, s43
	v_lshl_add_u64 v[202:203], s[34:35], 0, v[0:1]
	s_mov_b32 m0, s2
	ds_read_b128 v[168:171], v181 offset:16384
	ds_read_b128 v[172:175], v181 offset:17408
	ds_read_b128 v[176:179], v181 offset:18432
	ds_read_b128 v[182:185], v181 offset:19456
	ds_read_b128 v[186:189], v181 offset:20480
	ds_read_b128 v[190:193], v181 offset:21504
	ds_read_b128 v[194:197], v181 offset:22528
	ds_read_b128 v[198:201], v181 offset:23552
	global_load_lds_dwordx4 v[202:203], off
	s_add_i32 m0, s2, 0x2000
	s_add_u32 s28, s34, 0x40000
	v_lshl_add_u64 v[204:205], s[34:35], 0, v[130:131]
	s_addc_u32 s29, s35, 0
	s_add_i32 s2, s64, s43
	global_load_lds_dwordx4 v[204:205], off
	v_lshl_add_u64 v[206:207], s[28:29], 0, v[0:1]
	s_mov_b32 m0, s2
	v_lshl_add_u64 v[208:209], s[36:37], 0, v[130:131]
	global_load_lds_dwordx4 v[206:207], off
	v_lshl_add_u64 v[206:207], s[28:29], 0, v[130:131]
	s_add_i32 m0, s2, 0x2000
	s_nop 0
	global_load_lds_dwordx4 v[206:207], off
	v_lshl_add_u64 v[206:207], s[36:37], 0, v[0:1]
	s_mov_b32 m0, s44
	s_nop 0
	global_load_lds_dwordx4 v[206:207], off
	s_mov_b32 m0, s45
	s_nop 0
	global_load_lds_dwordx4 v[208:209], off
	s_waitcnt vmcnt(8)
	s_waitcnt lgkmcnt(0)
	s_barrier
; #define PG8_STAGE(bufoff, gbase, voff) do { _Pragma("unroll") for (int _i = 0; _i < 2; ++_i) \
;         __builtin_amdgcn_global_load_lds((const unsigned*)((const char*)(gbase) + (voff)[_i]), (PG8_LAS unsigned*)(lds + (bufoff) + ldsw + _i * 8192), 16, 0, 0); } while (0)
; #define PG8_LDA(dst, b, h) do { _Pragma("unroll") for (int m = 0; m < 4; ++m) _Pragma("unroll") for (int k = 0; k < 2; ++k) dst[m][k] = *(const PG8_LAS bf16x8*)(lds + PG8_SA(b, h) + aoff + m * 2048 + k * 1024); } while (0)
; #define PG8_LDB(dst, b, h) do { _Pragma("unroll") for (int n = 0; n < 2; ++n) _Pragma("unroll") for (int k = 0; k < 2; ++k) dst[n][k] = *(const PG8_LAS bf16x8*)(lds + PG8_SB(b, h) + boff + n * 2048 + k * 1024); } while (0)
; #define PG8_MMA(ai, bj, At, Bt) do { __builtin_amdgcn_s_setprio(1); _Pragma("unroll") for (int m = 0; m < 4; ++m) _Pragma("unroll") for (int n = 0; n < 2; ++n) _Pragma("unroll") for (int k = 0; k < 2; ++k) \
;         acc[ai][bj][m][n] = __builtin_amdgcn_mfma_f32_16x16x32_bf16(Bt[n][k], At[m][k], acc[ai][bj][m][n], 0, 0, 0); __builtin_amdgcn_s_setprio(0); } while (0)
; #define PG8_WAIT_V(n) asm volatile("s_waitcnt vmcnt(" #n ")" ::: "memory")
; #define PG8_WAIT_L(n) asm volatile("s_waitcnt lgkmcnt(" #n ")" ::: "memory")
; #define PG8_BAR __builtin_amdgcn_s_barrier()
; #define PG8_SCHED __builtin_amdgcn_sched_barrier(0)
; template <class Epi, class Sched, bool ALIGN_EPI = false, bool SP2 = false, bool GATHER = false>
; __device__ __forceinline__ void gemm_phase(PG8_LAS unsigned char* lds, const Gemm g, const Sched& S, const Epi& E, const int2* gslot = nullptr, PG8_LAS unsigned char* gtab = nullptr) {
;     ...
;             PG8_WAIT_V(8); PG8_WAIT_L(0); PG8_BAR; PG8_MMA(1, 0, At, B0); PG8_MMA(1, 1, At, B1); PG8_BAR; PG8_SCHED;
;             PG8_LDB(B0, 1, 0); PG8_LDB(B1, 1, 1); PG8_SCHED; PG8_LDA(At, 1, 0); PG8_STAGE(PG8_SA(0, 1), a2 + PG8_AH(1), PG8_VA(vS, 1));
;             PG8_WAIT_V(8); PG8_WAIT_L(0); PG8_BAR; PG8_MMA(0, 0, At, B0); PG8_MMA(0, 1, At, B1); PG8_BAR; PG8_SCHED;
	s_setprio 1
	v_mfma_f32_16x16x32_bf16 v[62:65], v[136:139], v[168:171], v[62:65]
	v_mfma_f32_16x16x32_bf16 v[58:61], v[144:147], v[168:171], v[58:61]
	v_mfma_f32_16x16x32_bf16 v[46:49], v[136:139], v[176:179], v[46:49]
	v_mfma_f32_16x16x32_bf16 v[42:45], v[144:147], v[176:179], v[42:45]
	v_mfma_f32_16x16x32_bf16 v[30:33], v[136:139], v[186:189], v[30:33]
	v_mfma_f32_16x16x32_bf16 v[26:29], v[144:147], v[186:189], v[26:29]
	v_mfma_f32_16x16x32_bf16 v[14:17], v[136:139], v[194:197], v[14:17]
	v_mfma_f32_16x16x32_bf16 v[10:13], v[144:147], v[194:197], v[10:13]
	v_mfma_f32_16x16x32_bf16 v[62:65], v[140:143], v[172:175], v[62:65]
	v_mfma_f32_16x16x32_bf16 v[58:61], v[148:151], v[172:175], v[58:61]
	v_mfma_f32_16x16x32_bf16 v[46:49], v[140:143], v[182:185], v[46:49]
	v_mfma_f32_16x16x32_bf16 v[42:45], v[148:151], v[182:185], v[42:45]
	v_mfma_f32_16x16x32_bf16 v[30:33], v[140:143], v[190:193], v[30:33]
	v_mfma_f32_16x16x32_bf16 v[26:29], v[148:151], v[190:193], v[26:29]
	v_mfma_f32_16x16x32_bf16 v[14:17], v[140:143], v[198:201], v[14:17]
	v_mfma_f32_16x16x32_bf16 v[10:13], v[148:151], v[198:201], v[10:13]
	v_mfma_f32_16x16x32_bf16 v[54:57], v[152:155], v[168:171], v[54:57]
	v_mfma_f32_16x16x32_bf16 v[50:53], v[160:163], v[168:171], v[50:53]
	v_mfma_f32_16x16x32_bf16 v[38:41], v[152:155], v[176:179], v[38:41]
	v_mfma_f32_16x16x32_bf16 v[34:37], v[160:163], v[176:179], v[34:37]
	v_mfma_f32_16x16x32_bf16 v[22:25], v[152:155], v[186:189], v[22:25]
	v_mfma_f32_16x16x32_bf16 v[18:21], v[160:163], v[186:189], v[18:21]
	v_mfma_f32_16x16x32_bf16 v[6:9], v[152:155], v[194:197], v[6:9]
	v_mfma_f32_16x16x32_bf16 v[2:5], v[160:163], v[194:197], v[2:5]
	v_mfma_f32_16x16x32_bf16 v[54:57], v[156:159], v[172:175], v[54:57]
	v_mfma_f32_16x16x32_bf16 v[50:53], v[164:167], v[172:175], v[50:53]
	v_mfma_f32_16x16x32_bf16 v[38:41], v[156:159], v[182:185], v[38:41]
	v_mfma_f32_16x16x32_bf16 v[34:37], v[164:167], v[182:185], v[34:37]
	v_mfma_f32_16x16x32_bf16 v[22:25], v[156:159], v[190:193], v[22:25]
	v_mfma_f32_16x16x32_bf16 v[18:21], v[164:167], v[190:193], v[18:21]
	v_mfma_f32_16x16x32_bf16 v[6:9], v[156:159], v[198:201], v[6:9]
	v_mfma_f32_16x16x32_bf16 v[2:5], v[164:167], v[198:201], v[2:5]
	s_setprio 0
	s_barrier
	s_add_i32 s2, 0, 0x18000
	s_add_i32 s64, 0, 0x1c000
	v_add_u32_e32 v148, s2, v215
	v_add_u32_e32 v164, s64, v215
	ds_read_b128 v[136:139], v148
	ds_read_b128 v[140:143], v148 offset:1024
	ds_read_b128 v[144:147], v148 offset:2048
	ds_read_b128 v[148:151], v148 offset:3072
	ds_read_b128 v[152:155], v164
	ds_read_b128 v[156:159], v164 offset:1024
	ds_read_b128 v[160:163], v164 offset:2048
	ds_read_b128 v[164:167], v164 offset:3072
	s_add_u32 s28, s36, 0x40000
	s_addc_u32 s29, s37, 0
	s_mov_b32 m0, s46
	v_lshl_add_u64 v[210:211], s[28:29], 0, v[0:1]
	ds_read_b128 v[168:171], v181 offset:32768
	ds_read_b128 v[172:175], v181 offset:33792
	ds_read_b128 v[176:179], v181 offset:34816
	ds_read_b128 v[182:185], v181 offset:35840
	ds_read_b128 v[186:189], v181 offset:36864
	ds_read_b128 v[190:193], v181 offset:37888
	ds_read_b128 v[194:197], v181 offset:38912
	ds_read_b128 v[198:201], v181 offset:39936
	global_load_lds_dwordx4 v[210:211], off
	v_lshl_add_u64 v[210:211], s[28:29], 0, v[130:131]
	s_mov_b32 m0, s47
	s_nop 0
	global_load_lds_dwordx4 v[210:211], off
	s_waitcnt vmcnt(8)
	s_waitcnt lgkmcnt(0)
	s_barrier
	s_setprio 1
	v_mfma_f32_16x16x32_bf16 v[126:129], v[136:139], v[168:171], v[126:129]
	v_mfma_f32_16x16x32_bf16 v[122:125], v[144:147], v[168:171], v[122:125]
	v_mfma_f32_16x16x32_bf16 v[110:113], v[136:139], v[176:179], v[110:113]
	v_mfma_f32_16x16x32_bf16 v[106:109], v[144:147], v[176:179], v[106:109]
	v_mfma_f32_16x16x32_bf16 v[94:97], v[136:139], v[186:189], v[94:97]
	v_mfma_f32_16x16x32_bf16 v[90:93], v[144:147], v[186:189], v[90:93]
	v_mfma_f32_16x16x32_bf16 v[78:81], v[136:139], v[194:197], v[78:81]
	v_mfma_f32_16x16x32_bf16 v[74:77], v[144:147], v[194:197], v[74:77]
	v_mfma_f32_16x16x32_bf16 v[126:129], v[140:143], v[172:175], v[126:129]
	v_mfma_f32_16x16x32_bf16 v[122:125], v[148:151], v[172:175], v[122:125]
	v_mfma_f32_16x16x32_bf16 v[110:113], v[140:143], v[182:185], v[110:113]
	v_mfma_f32_16x16x32_bf16 v[106:109], v[148:151], v[182:185], v[106:109]
	v_mfma_f32_16x16x32_bf16 v[94:97], v[140:143], v[190:193], v[94:97]
	v_mfma_f32_16x16x32_bf16 v[90:93], v[148:151], v[190:193], v[90:93]
	v_mfma_f32_16x16x32_bf16 v[78:81], v[140:143], v[198:201], v[78:81]
	v_mfma_f32_16x16x32_bf16 v[74:77], v[148:151], v[198:201], v[74:77]
	v_mfma_f32_16x16x32_bf16 v[118:121], v[152:155], v[168:171], v[118:121]
	v_mfma_f32_16x16x32_bf16 v[114:117], v[160:163], v[168:171], v[114:117]
	v_mfma_f32_16x16x32_bf16 v[102:105], v[152:155], v[176:179], v[102:105]
	v_mfma_f32_16x16x32_bf16 v[98:101], v[160:163], v[176:179], v[98:101]
	v_mfma_f32_16x16x32_bf16 v[86:89], v[152:155], v[186:189], v[86:89]
	v_mfma_f32_16x16x32_bf16 v[82:85], v[160:163], v[186:189], v[82:85]
	v_mfma_f32_16x16x32_bf16 v[70:73], v[152:155], v[194:197], v[70:73]
	v_mfma_f32_16x16x32_bf16 v[66:69], v[160:163], v[194:197], v[66:69]
	v_mfma_f32_16x16x32_bf16 v[118:121], v[156:159], v[172:175], v[118:121]
	v_mfma_f32_16x16x32_bf16 v[114:117], v[164:167], v[172:175], v[114:117]
	v_mfma_f32_16x16x32_bf16 v[102:105], v[156:159], v[182:185], v[102:105]
	v_mfma_f32_16x16x32_bf16 v[98:101], v[164:167], v[182:185], v[98:101]
	v_mfma_f32_16x16x32_bf16 v[86:89], v[156:159], v[190:193], v[86:89]
	v_mfma_f32_16x16x32_bf16 v[82:85], v[164:167], v[190:193], v[82:85]
	v_mfma_f32_16x16x32_bf16 v[70:73], v[156:159], v[198:201], v[70:73]
	v_mfma_f32_16x16x32_bf16 v[66:69], v[164:167], v[198:201], v[66:69]
	s_setprio 0
	s_barrier
; #define PG8_STAGE(bufoff, gbase, voff) do { _Pragma("unroll") for (int _i = 0; _i < 2; ++_i) \
;         __builtin_amdgcn_global_load_lds((const unsigned*)((const char*)(gbase) + (voff)[_i]), (PG8_LAS unsigned*)(lds + (bufoff) + ldsw + _i * 8192), 16, 0, 0); } while (0)
; #define PG8_LDA(dst, b, h) do { _Pragma("unroll") for (int m = 0; m < 4; ++m) _Pragma("unroll") for (int k = 0; k < 2; ++k) dst[m][k] = *(const PG8_LAS bf16x8*)(lds + PG8_SA(b, h) + aoff + m * 2048 + k * 1024); } while (0)
; #define PG8_MMA(ai, bj, At, Bt) do { __builtin_amdgcn_s_setprio(1); _Pragma("unroll") for (int m = 0; m < 4; ++m) _Pragma("unroll") for (int n = 0; n < 2; ++n) _Pragma("unroll") for (int k = 0; k < 2; ++k) \
;         acc[ai][bj][m][n] = __builtin_amdgcn_mfma_f32_16x16x32_bf16(Bt[n][k], At[m][k], acc[ai][bj][m][n], 0, 0, 0); __builtin_amdgcn_s_setprio(0); } while (0)
; #define PG8_WAIT_V(n) asm volatile("s_waitcnt vmcnt(" #n ")" ::: "memory")
; #define PG8_WAIT_L(n) asm volatile("s_waitcnt lgkmcnt(" #n ")" ::: "memory")
; #define PG8_BAR __builtin_amdgcn_s_barrier()
; #define PG8_SCHED __builtin_amdgcn_sched_barrier(0)
; template <class Epi, class Sched, bool ALIGN_EPI = false, bool SP2 = false, bool GATHER = false>
; __device__ __forceinline__ void gemm_phase(PG8_LAS unsigned char* lds, const Gemm g, const Sched& S, const Epi& E, const int2* gslot = nullptr, PG8_LAS unsigned char* gtab = nullptr) {
;     ...
;             PG8_LDA(At, 1, 1); PG8_STAGE(PG8_SB(1, 0), b3, voffB); PG8_STAGE(PG8_SB(1, 1), b3 + hstep, voffB); PG8_STAGE(PG8_SA(1, 0), a3, PG8_VA(vS, 0));
;             PG8_WAIT_V(8); PG8_WAIT_L(0); PG8_BAR; PG8_MMA(1, 0, At, B0); PG8_MMA(1, 1, At, B1); PG8_BAR; PG8_SCHED;
;     ...
;         if constexpr (ALIGN_EPI) { if (wr == 0) PG8_BAR; }
	s_add_i32 s2, s2, s43
	v_lshl_add_u64 v[202:203], v[202:203], 0, s[54:55]
	s_mov_b32 m0, s2
	ds_read_b128 v[168:171], v181 offset:49152
	ds_read_b128 v[172:175], v181 offset:50176
	ds_read_b128 v[176:179], v181 offset:51200
	ds_read_b128 v[182:185], v181 offset:52224
	ds_read_b128 v[186:189], v181 offset:53248
	ds_read_b128 v[190:193], v181 offset:54272
	ds_read_b128 v[194:197], v181 offset:55296
	ds_read_b128 v[198:201], v181 offset:56320
	global_load_lds_dwordx4 v[202:203], off
	s_add_i32 m0, s2, 0x2000
	s_add_u32 s28, s34, 0x40080
	v_lshl_add_u64 v[202:203], v[204:205], 0, s[54:55]
	s_addc_u32 s29, s35, 0
	s_add_i32 s2, s64, s43
	global_load_lds_dwordx4 v[202:203], off
	v_lshl_add_u64 v[202:203], s[28:29], 0, v[0:1]
	s_mov_b32 m0, s2
	s_nop 0
	global_load_lds_dwordx4 v[202:203], off
	v_lshl_add_u64 v[202:203], s[28:29], 0, v[130:131]
	s_add_i32 m0, s2, 0x2000
	s_nop 0
	global_load_lds_dwordx4 v[202:203], off
	v_lshl_add_u64 v[202:203], v[206:207], 0, s[54:55]
	s_mov_b32 m0, s50
	s_nop 0
	global_load_lds_dwordx4 v[202:203], off
	v_lshl_add_u64 v[202:203], v[208:209], 0, s[54:55]
	s_mov_b32 m0, s51
	s_nop 0
	global_load_lds_dwordx4 v[202:203], off
	s_waitcnt vmcnt(8)
	s_waitcnt lgkmcnt(0)
	s_barrier
	s_setprio 1
	v_mfma_f32_16x16x32_bf16 v[62:65], v[136:139], v[168:171], v[62:65]
	v_mfma_f32_16x16x32_bf16 v[58:61], v[144:147], v[168:171], v[58:61]
	v_mfma_f32_16x16x32_bf16 v[46:49], v[136:139], v[176:179], v[46:49]
	v_mfma_f32_16x16x32_bf16 v[42:45], v[144:147], v[176:179], v[42:45]
	v_mfma_f32_16x16x32_bf16 v[30:33], v[136:139], v[186:189], v[30:33]
	v_mfma_f32_16x16x32_bf16 v[26:29], v[144:147], v[186:189], v[26:29]
	v_mfma_f32_16x16x32_bf16 v[14:17], v[136:139], v[194:197], v[14:17]
	v_mfma_f32_16x16x32_bf16 v[10:13], v[144:147], v[194:197], v[10:13]
	v_mfma_f32_16x16x32_bf16 v[62:65], v[140:143], v[172:175], v[62:65]
	v_mfma_f32_16x16x32_bf16 v[58:61], v[148:151], v[172:175], v[58:61]
	v_mfma_f32_16x16x32_bf16 v[46:49], v[140:143], v[182:185], v[46:49]
	v_mfma_f32_16x16x32_bf16 v[42:45], v[148:151], v[182:185], v[42:45]
	v_mfma_f32_16x16x32_bf16 v[30:33], v[140:143], v[190:193], v[30:33]
	v_mfma_f32_16x16x32_bf16 v[26:29], v[148:151], v[190:193], v[26:29]
	v_mfma_f32_16x16x32_bf16 v[14:17], v[140:143], v[198:201], v[14:17]
	v_mfma_f32_16x16x32_bf16 v[10:13], v[148:151], v[198:201], v[10:13]
	v_mfma_f32_16x16x32_bf16 v[54:57], v[152:155], v[168:171], v[54:57]
	v_mfma_f32_16x16x32_bf16 v[50:53], v[160:163], v[168:171], v[50:53]
	v_mfma_f32_16x16x32_bf16 v[38:41], v[152:155], v[176:179], v[38:41]
	v_mfma_f32_16x16x32_bf16 v[34:37], v[160:163], v[176:179], v[34:37]
	v_mfma_f32_16x16x32_bf16 v[22:25], v[152:155], v[186:189], v[22:25]
	v_mfma_f32_16x16x32_bf16 v[18:21], v[160:163], v[186:189], v[18:21]
	v_mfma_f32_16x16x32_bf16 v[6:9], v[152:155], v[194:197], v[6:9]
	v_mfma_f32_16x16x32_bf16 v[2:5], v[160:163], v[194:197], v[2:5]
	v_mfma_f32_16x16x32_bf16 v[54:57], v[156:159], v[172:175], v[54:57]
	v_mfma_f32_16x16x32_bf16 v[50:53], v[164:167], v[172:175], v[50:53]
	v_mfma_f32_16x16x32_bf16 v[38:41], v[156:159], v[182:185], v[38:41]
	v_mfma_f32_16x16x32_bf16 v[34:37], v[164:167], v[182:185], v[34:37]
	v_mfma_f32_16x16x32_bf16 v[22:25], v[156:159], v[190:193], v[22:25]
	v_mfma_f32_16x16x32_bf16 v[18:21], v[164:167], v[190:193], v[18:21]
	v_mfma_f32_16x16x32_bf16 v[6:9], v[156:159], v[198:201], v[6:9]
	v_mfma_f32_16x16x32_bf16 v[2:5], v[164:167], v[198:201], v[2:5]
	s_setprio 0
	s_barrier
	s_add_i32 s63, s63, 2
	s_add_u32 s61, s61, 0x100
	s_addc_u32 s62, s62, 0
	s_cmp_gt_u32 s63, 13
	s_mov_b64 s[28:29], s[30:31]
	s_cbranch_scc0 .LBB0_813
	s_and_b64 vcc, exec, s[18:19]
	s_cbranch_vccz .LBB0_816
	s_barrier

; #define PG8_GREAD(dst, u, par) do { _Pragma("unroll") for (int h_ = 0; h_ < 2; ++h_) _Pragma("unroll") for (int i_ = 0; i_ < 2; ++i_) { const int rl_ = 128 * h_ + grl[i_]; \
;         const int tk_ = *(const PG8_LAS int*)(gtab + (par) * 2048 + rl_ * 8); const unsigned tok_ = (rl_ < (u).rows) ? ((unsigned)tk_ >> 2) : 0u; dst[h_][i_] = tok_ * (unsigned)(K * 2) + gcb[i_]; } } while (0)
; #define PG8_STAGE(bufoff, gbase, voff) do { _Pragma("unroll") for (int _i = 0; _i < 2; ++_i) \
;         __builtin_amdgcn_global_load_lds((const unsigned*)((const char*)(gbase) + (voff)[_i]), (PG8_LAS unsigned*)(lds + (bufoff) + ldsw + _i * 8192), 16, 0, 0); } while (0)
; #define PG8_LDA(dst, b, h) do { _Pragma("unroll") for (int m = 0; m < 4; ++m) _Pragma("unroll") for (int k = 0; k < 2; ++k) dst[m][k] = *(const PG8_LAS bf16x8*)(lds + PG8_SA(b, h) + aoff + m * 2048 + k * 1024); } while (0)
; template <class Epi, class Sched, bool ALIGN_EPI = false, bool SP2 = false, bool GATHER = false>
; __device__ __forceinline__ void gemm_phase(PG8_LAS unsigned char* lds, const Gemm g, const Sched& S, const Epi& E, const int2* gslot = nullptr, PG8_LAS unsigned char* gtab = nullptr) {
;     ...
;             const char* a1 = cA + (size_t)(t + 1) * kstep;
;             const char* a2 = last ? nA : cA + (size_t)(t + 2) * kstep; const char* b2 = last ? nB : cB + (size_t)(t + 2) * kstep;
;             const char* a3 = a2 + kstep; const char* b3 = b2 + kstep;
;             if (last && has_next) S.a_ready(nxt);
;             if constexpr (GATHER) { if (last) { if (has_next) { PG8_GREAD(vN, nxt, (ui + 1) & 1); } else { _Pragma("unroll") for (int h_ = 0; h_ < 2; ++h_) _Pragma("unroll") for (int i_ = 0; i_ < 2; ++i_) vN[h_][i_] = vC[h_][i_]; } } }
;             unsigned vS[2][2];
; #pragma unroll
;             for (int h_ = 0; h_ < 2; ++h_)
; #pragma unroll
;                 for (int i_ = 0; i_ < 2; ++i_) vS[h_][i_] = (GATHER && last) ? vN[h_][i_] : vC[h_][i_];
;             if constexpr (SP2) {
;             PG8_LDB(B0, 0, 0); PG8_LDB(B1, 0, 1); PG8_SCHED; PG8_LDA(At, 0, 0); PG8_STAGE(PG8_SA(1, 1), a1 + PG8_AH(1), PG8_VA(vC, 1));
;             PG8_WAIT_V(8); PG8_WAIT_L(0); PG8_BAR; PG8_MMA(0, 0, At, B0); PG8_MMA(0, 1, At, B1); PG8_BAR; PG8_SCHED;
;             PG8_LDA(At, 0, 1); PG8_STAGE(PG8_SB(0, 0), b2, voffB); PG8_STAGE(PG8_SB(0, 1), b2 + hstep, voffB); PG8_STAGE(PG8_SA(0, 0), a2, PG8_VA(vS, 0));
.LBB0_1093:
	s_add_u32 s70, s18, s60
	s_addc_u32 s71, s19, s61
	s_add_u32 vcc_lo, s70, 0x34000100
	s_addc_u32 vcc_hi, s71, 0
	s_and_b64 s[70:71], s[72:73], exec
	s_cselect_b32 s71, s25, vcc_hi
	s_cselect_b32 s70, s24, vcc_lo
	s_add_u32 vcc_lo, s21, s60
	s_addc_u32 vcc_hi, s37, s61
	s_and_b64 s[72:73], s[72:73], exec
	s_cselect_b32 vcc_hi, s53, vcc_hi
	s_cselect_b32 vcc_lo, s52, vcc_lo
	s_add_i32 s72, 0, 0x10000
	v_add_u32_e32 v139, s72, v155
	s_add_i32 s2, 0, 0x14000
	ds_read_b128 v[140:143], v139
	ds_read_b128 v[162:165], v139 offset:1024
	ds_read_b128 v[180:183], v139 offset:2048
	ds_read_b128 v[188:191], v139 offset:3072
	v_add_u32_e32 v139, s2, v155
	ds_read_b128 v[192:195], v139
	ds_read_b128 v[196:199], v139 offset:1024
	ds_read_b128 v[200:203], v139 offset:2048
	ds_read_b128 v[204:207], v139 offset:3072
	v_lshl_add_u64 v[144:145], v[132:133], 0, s[60:61]
	s_add_i32 m0, s97, 0xc000
	ds_read_b128 v[208:211], v184
	ds_read_b128 v[212:215], v184 offset:1024
	ds_read_b128 v[216:219], v184 offset:2048
	ds_read_b128 v[220:223], v184 offset:3072
	ds_read_b128 v[224:227], v184 offset:4096
	ds_read_b128 v[230:233], v184 offset:5120
	ds_read_b128 v[236:239], v184 offset:6144
	ds_read_b128 v[240:243], v184 offset:7168
	global_load_lds_dwordx4 v[144:145], off
	v_lshl_add_u64 v[144:145], v[130:131], 0, s[60:61]
	s_add_i32 m0, s97, 0xe000
	s_nop 0
	global_load_lds_dwordx4 v[144:145], off
	s_waitcnt vmcnt(8)
	s_waitcnt lgkmcnt(0)
	s_barrier
	s_setprio 1
	v_mfma_f32_16x16x32_bf16 v[122:125], v[140:143], v[208:211], v[122:125]
	v_mfma_f32_16x16x32_bf16 v[114:117], v[180:183], v[208:211], v[114:117]
	v_mfma_f32_16x16x32_bf16 v[106:109], v[140:143], v[216:219], v[106:109]
	v_mfma_f32_16x16x32_bf16 v[98:101], v[180:183], v[216:219], v[98:101]
	v_mfma_f32_16x16x32_bf16 v[94:97], v[140:143], v[224:227], v[94:97]
	v_mfma_f32_16x16x32_bf16 v[90:93], v[180:183], v[224:227], v[90:93]
	v_mfma_f32_16x16x32_bf16 v[86:89], v[140:143], v[236:239], v[86:89]
	v_mfma_f32_16x16x32_bf16 v[82:85], v[180:183], v[236:239], v[82:85]
	v_mfma_f32_16x16x32_bf16 v[122:125], v[162:165], v[212:215], v[122:125]
	v_mfma_f32_16x16x32_bf16 v[114:117], v[188:191], v[212:215], v[114:117]
	v_mfma_f32_16x16x32_bf16 v[106:109], v[162:165], v[220:223], v[106:109]
	v_mfma_f32_16x16x32_bf16 v[98:101], v[188:191], v[220:223], v[98:101]
	v_mfma_f32_16x16x32_bf16 v[94:97], v[162:165], v[230:233], v[94:97]
	v_mfma_f32_16x16x32_bf16 v[90:93], v[188:191], v[230:233], v[90:93]
	v_mfma_f32_16x16x32_bf16 v[86:89], v[162:165], v[240:243], v[86:89]
	v_mfma_f32_16x16x32_bf16 v[82:85], v[188:191], v[240:243], v[82:85]
	v_mfma_f32_16x16x32_bf16 v[78:81], v[192:195], v[208:211], v[78:81]
	v_mfma_f32_16x16x32_bf16 v[74:77], v[200:203], v[208:211], v[74:77]
	v_mfma_f32_16x16x32_bf16 v[70:73], v[192:195], v[216:219], v[70:73]
	v_mfma_f32_16x16x32_bf16 v[66:69], v[200:203], v[216:219], v[66:69]
	v_mfma_f32_16x16x32_bf16 v[62:65], v[192:195], v[224:227], v[62:65]
	v_mfma_f32_16x16x32_bf16 v[58:61], v[200:203], v[224:227], v[58:61]
	v_mfma_f32_16x16x32_bf16 v[54:57], v[192:195], v[236:239], v[54:57]
	v_mfma_f32_16x16x32_bf16 v[50:53], v[200:203], v[236:239], v[50:53]
	v_mfma_f32_16x16x32_bf16 v[78:81], v[196:199], v[212:215], v[78:81]
	v_mfma_f32_16x16x32_bf16 v[74:77], v[204:207], v[212:215], v[74:77]
	v_mfma_f32_16x16x32_bf16 v[70:73], v[196:199], v[220:223], v[70:73]
	v_mfma_f32_16x16x32_bf16 v[66:69], v[204:207], v[220:223], v[66:69]
	v_mfma_f32_16x16x32_bf16 v[62:65], v[196:199], v[230:233], v[62:65]
	v_mfma_f32_16x16x32_bf16 v[58:61], v[204:207], v[230:233], v[58:61]
	v_mfma_f32_16x16x32_bf16 v[54:57], v[196:199], v[240:243], v[54:57]
	v_mfma_f32_16x16x32_bf16 v[50:53], v[204:207], v[240:243], v[50:53]
	s_setprio 0
	s_barrier
	s_add_i32 s72, s72, s47
	v_lshl_add_u64 v[166:167], vcc, 0, v[148:149]
	s_mov_b32 m0, s72
	ds_read_b128 v[208:211], v184 offset:16384
	ds_read_b128 v[212:215], v184 offset:17408
	ds_read_b128 v[216:219], v184 offset:18432
	ds_read_b128 v[220:223], v184 offset:19456
	ds_read_b128 v[224:227], v184 offset:20480
	ds_read_b128 v[230:233], v184 offset:21504
	ds_read_b128 v[236:239], v184 offset:22528
	ds_read_b128 v[240:243], v184 offset:23552
	global_load_lds_dwordx4 v[166:167], off
	s_add_i32 m0, s72, 0x2000
	s_add_u32 s72, vcc_lo, 0x40000
	v_lshl_add_u64 v[244:245], vcc, 0, v[150:151]
	s_addc_u32 s73, vcc_hi, 0
	s_add_i32 s2, s2, s47
	global_load_lds_dwordx4 v[244:245], off
	v_lshl_add_u64 v[144:145], s[72:73], 0, v[148:149]
	s_mov_b32 m0, s2
	v_mov_b32_e32 v139, v1
	global_load_lds_dwordx4 v[144:145], off
	v_lshl_add_u64 v[144:145], s[72:73], 0, v[150:151]
	s_add_i32 m0, s2, 0x2000
	v_lshl_add_u64 v[246:247], s[70:71], 0, v[0:1]
	global_load_lds_dwordx4 v[144:145], off
	s_mov_b32 m0, s97
	v_lshl_add_u64 v[248:249], s[70:71], 0, v[138:139]
	global_load_lds_dwordx4 v0, s[70:71]
	s_mov_b32 m0, s66
	s_nop 0
	global_load_lds_dwordx4 v138, s[70:71]
	s_waitcnt vmcnt(8)
	s_waitcnt lgkmcnt(0)
	s_barrier
; #define PG8_STAGE(bufoff, gbase, voff) do { _Pragma("unroll") for (int _i = 0; _i < 2; ++_i) \
;         __builtin_amdgcn_global_load_lds((const unsigned*)((const char*)(gbase) + (voff)[_i]), (PG8_LAS unsigned*)(lds + (bufoff) + ldsw + _i * 8192), 16, 0, 0); } while (0)
; #define PG8_LDA(dst, b, h) do { _Pragma("unroll") for (int m = 0; m < 4; ++m) _Pragma("unroll") for (int k = 0; k < 2; ++k) dst[m][k] = *(const PG8_LAS bf16x8*)(lds + PG8_SA(b, h) + aoff + m * 2048 + k * 1024); } while (0)
; #define PG8_LDB(dst, b, h) do { _Pragma("unroll") for (int n = 0; n < 2; ++n) _Pragma("unroll") for (int k = 0; k < 2; ++k) dst[n][k] = *(const PG8_LAS bf16x8*)(lds + PG8_SB(b, h) + boff + n * 2048 + k * 1024); } while (0)
; #define PG8_MMA(ai, bj, At, Bt) do { __builtin_amdgcn_s_setprio(1); _Pragma("unroll") for (int m = 0; m < 4; ++m) _Pragma("unroll") for (int n = 0; n < 2; ++n) _Pragma("unroll") for (int k = 0; k < 2; ++k) \
;         acc[ai][bj][m][n] = __builtin_amdgcn_mfma_f32_16x16x32_bf16(Bt[n][k], At[m][k], acc[ai][bj][m][n], 0, 0, 0); __builtin_amdgcn_s_setprio(0); } while (0)
; #define PG8_WAIT_V(n) asm volatile("s_waitcnt vmcnt(" #n ")" ::: "memory")
; #define PG8_WAIT_L(n) asm volatile("s_waitcnt lgkmcnt(" #n ")" ::: "memory")
; #define PG8_BAR __builtin_amdgcn_s_barrier()
; #define PG8_SCHED __builtin_amdgcn_sched_barrier(0)
; template <class Epi, class Sched, bool ALIGN_EPI = false, bool SP2 = false, bool GATHER = false>
; __device__ __forceinline__ void gemm_phase(PG8_LAS unsigned char* lds, const Gemm g, const Sched& S, const Epi& E, const int2* gslot = nullptr, PG8_LAS unsigned char* gtab = nullptr) {
;     ...
;             PG8_LDA(At, 0, 1); PG8_STAGE(PG8_SB(0, 0), b2, voffB); PG8_STAGE(PG8_SB(0, 1), b2 + hstep, voffB); PG8_STAGE(PG8_SA(0, 0), a2, PG8_VA(vS, 0));
;             PG8_WAIT_V(8); PG8_WAIT_L(0); PG8_BAR; PG8_MMA(1, 0, At, B0); PG8_MMA(1, 1, At, B1); PG8_BAR; PG8_SCHED;
;             PG8_LDB(B0, 1, 0); PG8_LDB(B1, 1, 1); PG8_SCHED; PG8_LDA(At, 1, 0); PG8_STAGE(PG8_SA(0, 1), a2 + PG8_AH(1), PG8_VA(vS, 1));
;             PG8_WAIT_V(8); PG8_WAIT_L(0); PG8_BAR; PG8_MMA(0, 0, At, B0); PG8_MMA(0, 1, At, B1); PG8_BAR; PG8_SCHED;
	s_setprio 1
	v_mfma_f32_16x16x32_bf16 v[46:49], v[140:143], v[208:211], v[46:49]
	v_mfma_f32_16x16x32_bf16 v[42:45], v[180:183], v[208:211], v[42:45]
	v_mfma_f32_16x16x32_bf16 v[38:41], v[140:143], v[216:219], v[38:41]
	v_mfma_f32_16x16x32_bf16 v[34:37], v[180:183], v[216:219], v[34:37]
	v_mfma_f32_16x16x32_bf16 v[30:33], v[140:143], v[224:227], v[30:33]
	v_mfma_f32_16x16x32_bf16 v[26:29], v[180:183], v[224:227], v[26:29]
	v_mfma_f32_16x16x32_bf16 v[6:9], v[140:143], v[236:239], v[6:9]
	v_mfma_f32_16x16x32_bf16 v[2:5], v[180:183], v[236:239], v[2:5]
	v_mfma_f32_16x16x32_bf16 v[46:49], v[162:165], v[212:215], v[46:49]
	v_mfma_f32_16x16x32_bf16 v[42:45], v[188:191], v[212:215], v[42:45]
	v_mfma_f32_16x16x32_bf16 v[38:41], v[162:165], v[220:223], v[38:41]
	v_mfma_f32_16x16x32_bf16 v[34:37], v[188:191], v[220:223], v[34:37]
	v_mfma_f32_16x16x32_bf16 v[30:33], v[162:165], v[230:233], v[30:33]
	v_mfma_f32_16x16x32_bf16 v[26:29], v[188:191], v[230:233], v[26:29]
	v_mfma_f32_16x16x32_bf16 v[6:9], v[162:165], v[240:243], v[6:9]
	v_mfma_f32_16x16x32_bf16 v[2:5], v[188:191], v[240:243], v[2:5]
	v_mfma_f32_16x16x32_bf16 v[22:25], v[192:195], v[208:211], v[22:25]
	v_mfma_f32_16x16x32_bf16 v[18:21], v[200:203], v[208:211], v[18:21]
	v_mfma_f32_16x16x32_bf16 v[14:17], v[192:195], v[216:219], v[14:17]
	v_mfma_f32_16x16x32_bf16 v[10:13], v[200:203], v[216:219], v[10:13]
	v_mfma_f32_16x16x32_bf16 v[102:105], v[192:195], v[224:227], v[102:105]
	v_mfma_f32_16x16x32_bf16 v[110:113], v[200:203], v[224:227], v[110:113]
	v_mfma_f32_16x16x32_bf16 v[118:121], v[192:195], v[236:239], v[118:121]
	v_mfma_f32_16x16x32_bf16 v[126:129], v[200:203], v[236:239], v[126:129]
	v_mfma_f32_16x16x32_bf16 v[22:25], v[196:199], v[212:215], v[22:25]
	v_mfma_f32_16x16x32_bf16 v[18:21], v[204:207], v[212:215], v[18:21]
	v_mfma_f32_16x16x32_bf16 v[14:17], v[196:199], v[220:223], v[14:17]
	v_mfma_f32_16x16x32_bf16 v[10:13], v[204:207], v[220:223], v[10:13]
	v_mfma_f32_16x16x32_bf16 v[102:105], v[196:199], v[230:233], v[102:105]
	v_mfma_f32_16x16x32_bf16 v[110:113], v[204:207], v[230:233], v[110:113]
	v_mfma_f32_16x16x32_bf16 v[118:121], v[196:199], v[240:243], v[118:121]
	v_mfma_f32_16x16x32_bf16 v[126:129], v[204:207], v[240:243], v[126:129]
	s_setprio 0
	s_barrier
	s_add_i32 s2, 0, 0x18000
	v_add_u32_e32 v0, s2, v155
	s_add_i32 s72, 0, 0x1c000
	ds_read_b128 v[138:141], v0
	ds_read_b128 v[142:145], v0 offset:1024
	ds_read_b128 v[162:165], v0 offset:2048
	ds_read_b128 v[180:183], v0 offset:3072
	v_add_u32_e32 v0, s72, v155
	ds_read_b128 v[188:191], v0
	ds_read_b128 v[192:195], v0 offset:1024
	ds_read_b128 v[196:199], v0 offset:2048
	ds_read_b128 v[200:203], v0 offset:3072
	s_mov_b32 m0, s67
	v_lshl_add_u64 v[136:137], s[70:71], 0, v[136:137]
	ds_read_b128 v[204:207], v184 offset:32768
	ds_read_b128 v[208:211], v184 offset:33792
	ds_read_b128 v[212:215], v184 offset:34816
	ds_read_b128 v[216:219], v184 offset:35840
	ds_read_b128 v[220:223], v184 offset:36864
	ds_read_b128 v[224:227], v184 offset:37888
	ds_read_b128 v[230:233], v184 offset:38912
	ds_read_b128 v[236:239], v184 offset:39936
	global_load_lds_dwordx4 v[136:137], off
	v_lshl_add_u64 v[134:135], s[70:71], 0, v[134:135]
	s_mov_b32 m0, s56
	s_nop 0
	global_load_lds_dwordx4 v[134:135], off
	s_waitcnt vmcnt(8)
	s_waitcnt lgkmcnt(0)
	s_barrier
	s_setprio 1
	v_mfma_f32_16x16x32_bf16 v[122:125], v[138:141], v[204:207], v[122:125]
	v_mfma_f32_16x16x32_bf16 v[114:117], v[162:165], v[204:207], v[114:117]
	v_mfma_f32_16x16x32_bf16 v[106:109], v[138:141], v[212:215], v[106:109]
	v_mfma_f32_16x16x32_bf16 v[98:101], v[162:165], v[212:215], v[98:101]
	v_mfma_f32_16x16x32_bf16 v[94:97], v[138:141], v[220:223], v[94:97]
	v_mfma_f32_16x16x32_bf16 v[90:93], v[162:165], v[220:223], v[90:93]
	v_mfma_f32_16x16x32_bf16 v[86:89], v[138:141], v[230:233], v[86:89]
	v_mfma_f32_16x16x32_bf16 v[82:85], v[162:165], v[230:233], v[82:85]
	v_mfma_f32_16x16x32_bf16 v[122:125], v[142:145], v[208:211], v[122:125]
	v_mfma_f32_16x16x32_bf16 v[114:117], v[180:183], v[208:211], v[114:117]
	v_mfma_f32_16x16x32_bf16 v[106:109], v[142:145], v[216:219], v[106:109]
	v_mfma_f32_16x16x32_bf16 v[98:101], v[180:183], v[216:219], v[98:101]
	v_mfma_f32_16x16x32_bf16 v[94:97], v[142:145], v[224:227], v[94:97]
	v_mfma_f32_16x16x32_bf16 v[90:93], v[180:183], v[224:227], v[90:93]
	v_mfma_f32_16x16x32_bf16 v[86:89], v[142:145], v[236:239], v[86:89]
	v_mfma_f32_16x16x32_bf16 v[82:85], v[180:183], v[236:239], v[82:85]
	v_mfma_f32_16x16x32_bf16 v[78:81], v[188:191], v[204:207], v[78:81]
	v_mfma_f32_16x16x32_bf16 v[74:77], v[196:199], v[204:207], v[74:77]
	v_mfma_f32_16x16x32_bf16 v[70:73], v[188:191], v[212:215], v[70:73]
	v_mfma_f32_16x16x32_bf16 v[66:69], v[196:199], v[212:215], v[66:69]
	v_mfma_f32_16x16x32_bf16 v[62:65], v[188:191], v[220:223], v[62:65]
	v_mfma_f32_16x16x32_bf16 v[58:61], v[196:199], v[220:223], v[58:61]
	v_mfma_f32_16x16x32_bf16 v[54:57], v[188:191], v[230:233], v[54:57]
	v_mfma_f32_16x16x32_bf16 v[50:53], v[196:199], v[230:233], v[50:53]
	v_mfma_f32_16x16x32_bf16 v[78:81], v[192:195], v[208:211], v[78:81]
	v_mfma_f32_16x16x32_bf16 v[74:77], v[200:203], v[208:211], v[74:77]
	v_mfma_f32_16x16x32_bf16 v[70:73], v[192:195], v[216:219], v[70:73]
	v_mfma_f32_16x16x32_bf16 v[66:69], v[200:203], v[216:219], v[66:69]
	v_mfma_f32_16x16x32_bf16 v[62:65], v[192:195], v[224:227], v[62:65]
	v_mfma_f32_16x16x32_bf16 v[58:61], v[200:203], v[224:227], v[58:61]
	v_mfma_f32_16x16x32_bf16 v[54:57], v[192:195], v[236:239], v[54:57]
	v_mfma_f32_16x16x32_bf16 v[50:53], v[200:203], v[236:239], v[50:53]
	s_setprio 0
	s_barrier
; #define PG8_STAGE(bufoff, gbase, voff) do { _Pragma("unroll") for (int _i = 0; _i < 2; ++_i) \
;         __builtin_amdgcn_global_load_lds((const unsigned*)((const char*)(gbase) + (voff)[_i]), (PG8_LAS unsigned*)(lds + (bufoff) + ldsw + _i * 8192), 16, 0, 0); } while (0)
; #define PG8_LDA(dst, b, h) do { _Pragma("unroll") for (int m = 0; m < 4; ++m) _Pragma("unroll") for (int k = 0; k < 2; ++k) dst[m][k] = *(const PG8_LAS bf16x8*)(lds + PG8_SA(b, h) + aoff + m * 2048 + k * 1024); } while (0)
; #define PG8_MMA(ai, bj, At, Bt) do { __builtin_amdgcn_s_setprio(1); _Pragma("unroll") for (int m = 0; m < 4; ++m) _Pragma("unroll") for (int n = 0; n < 2; ++n) _Pragma("unroll") for (int k = 0; k < 2; ++k) \
;         acc[ai][bj][m][n] = __builtin_amdgcn_mfma_f32_16x16x32_bf16(Bt[n][k], At[m][k], acc[ai][bj][m][n], 0, 0, 0); __builtin_amdgcn_s_setprio(0); } while (0)
; #define PG8_WAIT_V(n) asm volatile("s_waitcnt vmcnt(" #n ")" ::: "memory")
; #define PG8_WAIT_L(n) asm volatile("s_waitcnt lgkmcnt(" #n ")" ::: "memory")
; #define PG8_BAR __builtin_amdgcn_s_barrier()
; #define PG8_SCHED __builtin_amdgcn_sched_barrier(0)
; template <class Epi, class Sched, bool ALIGN_EPI = false, bool SP2 = false, bool GATHER = false>
; __device__ __forceinline__ void gemm_phase(PG8_LAS unsigned char* lds, const Gemm g, const Sched& S, const Epi& E, const int2* gslot = nullptr, PG8_LAS unsigned char* gtab = nullptr) {
;     ...
;             PG8_LDA(At, 1, 1); PG8_STAGE(PG8_SB(1, 0), b3, voffB); PG8_STAGE(PG8_SB(1, 1), b3 + hstep, voffB); PG8_STAGE(PG8_SA(1, 0), a3, PG8_VA(vS, 0));
;             PG8_WAIT_V(8); PG8_WAIT_L(0); PG8_BAR; PG8_MMA(1, 0, At, B0); PG8_MMA(1, 1, At, B1); PG8_BAR; PG8_SCHED;
	s_add_i32 s2, s2, s47
	v_lshl_add_u64 v[166:167], v[166:167], 0, s[54:55]
	s_mov_b32 m0, s2
	ds_read_b128 v[134:137], v184 offset:49152
	ds_read_b128 v[204:207], v184 offset:50176
	ds_read_b128 v[208:211], v184 offset:51200
	ds_read_b128 v[212:215], v184 offset:52224
	ds_read_b128 v[216:219], v184 offset:53248
	ds_read_b128 v[220:223], v184 offset:54272
	ds_read_b128 v[224:227], v184 offset:55296
	ds_read_b128 v[230:233], v184 offset:56320
	global_load_lds_dwordx4 v[166:167], off
	s_add_i32 m0, s2, 0x2000
	s_add_u32 s70, vcc_lo, 0x40080
	v_lshl_add_u64 v[166:167], v[244:245], 0, s[54:55]
	s_addc_u32 s71, vcc_hi, 0
	s_add_i32 s2, s72, s47
	global_load_lds_dwordx4 v[166:167], off
	v_lshl_add_u64 v[166:167], s[70:71], 0, v[148:149]
	s_mov_b32 m0, s2
	s_nop 0
	global_load_lds_dwordx4 v[166:167], off
	v_lshl_add_u64 v[166:167], s[70:71], 0, v[150:151]
	s_add_i32 m0, s2, 0x2000
	s_nop 0
	global_load_lds_dwordx4 v[166:167], off
	v_lshl_add_u64 v[166:167], v[246:247], 0, s[54:55]
	s_mov_b32 m0, s0
	s_nop 0
	global_load_lds_dwordx4 v[166:167], off
	v_lshl_add_u64 v[166:167], v[248:249], 0, s[54:55]
	s_mov_b32 m0, s43
	s_nop 0
	global_load_lds_dwordx4 v[166:167], off
	s_waitcnt vmcnt(8)
	s_waitcnt lgkmcnt(0)
	s_barrier
	s_setprio 1
	v_mfma_f32_16x16x32_bf16 v[46:49], v[138:141], v[134:137], v[46:49]
	v_mfma_f32_16x16x32_bf16 v[42:45], v[162:165], v[134:137], v[42:45]
	v_mfma_f32_16x16x32_bf16 v[38:41], v[138:141], v[208:211], v[38:41]
	v_mfma_f32_16x16x32_bf16 v[34:37], v[162:165], v[208:211], v[34:37]
	v_mfma_f32_16x16x32_bf16 v[30:33], v[138:141], v[216:219], v[30:33]
	v_mfma_f32_16x16x32_bf16 v[26:29], v[162:165], v[216:219], v[26:29]
	v_mfma_f32_16x16x32_bf16 v[6:9], v[138:141], v[224:227], v[6:9]
	v_mfma_f32_16x16x32_bf16 v[2:5], v[162:165], v[224:227], v[2:5]
	v_mfma_f32_16x16x32_bf16 v[46:49], v[142:145], v[204:207], v[46:49]
	v_mfma_f32_16x16x32_bf16 v[42:45], v[180:183], v[204:207], v[42:45]
	v_mfma_f32_16x16x32_bf16 v[38:41], v[142:145], v[212:215], v[38:41]
	v_mfma_f32_16x16x32_bf16 v[34:37], v[180:183], v[212:215], v[34:37]
	v_mfma_f32_16x16x32_bf16 v[30:33], v[142:145], v[220:223], v[30:33]
	v_mfma_f32_16x16x32_bf16 v[26:29], v[180:183], v[220:223], v[26:29]
	v_mfma_f32_16x16x32_bf16 v[6:9], v[142:145], v[230:233], v[6:9]
	v_mfma_f32_16x16x32_bf16 v[2:5], v[180:183], v[230:233], v[2:5]
	v_mfma_f32_16x16x32_bf16 v[22:25], v[188:191], v[134:137], v[22:25]
	v_mfma_f32_16x16x32_bf16 v[18:21], v[196:199], v[134:137], v[18:21]
	v_mfma_f32_16x16x32_bf16 v[14:17], v[188:191], v[208:211], v[14:17]
	v_mfma_f32_16x16x32_bf16 v[10:13], v[196:199], v[208:211], v[10:13]
	v_mfma_f32_16x16x32_bf16 v[102:105], v[188:191], v[216:219], v[102:105]
	v_mfma_f32_16x16x32_bf16 v[110:113], v[196:199], v[216:219], v[110:113]
	v_mfma_f32_16x16x32_bf16 v[118:121], v[188:191], v[224:227], v[118:121]
	v_mfma_f32_16x16x32_bf16 v[126:129], v[196:199], v[224:227], v[126:129]
	v_mfma_f32_16x16x32_bf16 v[22:25], v[192:195], v[204:207], v[22:25]
	v_mfma_f32_16x16x32_bf16 v[18:21], v[200:203], v[204:207], v[18:21]
	v_mfma_f32_16x16x32_bf16 v[14:17], v[192:195], v[212:215], v[14:17]
	v_mfma_f32_16x16x32_bf16 v[10:13], v[200:203], v[212:215], v[10:13]
	v_mfma_f32_16x16x32_bf16 v[102:105], v[192:195], v[220:223], v[102:105]
	v_mfma_f32_16x16x32_bf16 v[110:113], v[200:203], v[220:223], v[110:113]
	v_mfma_f32_16x16x32_bf16 v[118:121], v[192:195], v[230:233], v[118:121]
	v_mfma_f32_16x16x32_bf16 v[126:129], v[200:203], v[230:233], v[126:129]
	s_setprio 0
	s_barrier
	s_add_i32 s69, s69, 2
	s_add_u32 s60, s60, 0x100
	s_addc_u32 s61, s61, 0
	s_cmp_gt_u32 s69, 13
	s_cbranch_scc1 .LBB0_1097

; #define PG8_GREAD(dst, u, par) do { _Pragma("unroll") for (int h_ = 0; h_ < 2; ++h_) _Pragma("unroll") for (int i_ = 0; i_ < 2; ++i_) { const int rl_ = 128 * h_ + grl[i_]; \
;         const int tk_ = *(const PG8_LAS int*)(gtab + (par) * 2048 + rl_ * 8); const unsigned tok_ = (rl_ < (u).rows) ? ((unsigned)tk_ >> 2) : 0u; dst[h_][i_] = tok_ * (unsigned)(K * 2) + gcb[i_]; } } while (0)
; #define PG8_STAGE(bufoff, gbase, voff) do { _Pragma("unroll") for (int _i = 0; _i < 2; ++_i) \
;         __builtin_amdgcn_global_load_lds((const unsigned*)((const char*)(gbase) + (voff)[_i]), (PG8_LAS unsigned*)(lds + (bufoff) + ldsw + _i * 8192), 16, 0, 0); } while (0)
; #define PG8_LDA(dst, b, h) do { _Pragma("unroll") for (int m = 0; m < 4; ++m) _Pragma("unroll") for (int k = 0; k < 2; ++k) dst[m][k] = *(const PG8_LAS bf16x8*)(lds + PG8_SA(b, h) + aoff + m * 2048 + k * 1024); } while (0)
; template <class Epi, class Sched, bool ALIGN_EPI = false, bool SP2 = false, bool GATHER = false>
; __device__ __forceinline__ void gemm_phase(PG8_LAS unsigned char* lds, const Gemm g, const Sched& S, const Epi& E, const int2* gslot = nullptr, PG8_LAS unsigned char* gtab = nullptr) {
;     ...
;             const char* a1 = cA + (size_t)(t + 1) * kstep;
;             const char* a2 = last ? nA : cA + (size_t)(t + 2) * kstep; const char* b2 = last ? nB : cB + (size_t)(t + 2) * kstep;
;             const char* a3 = a2 + kstep; const char* b3 = b2 + kstep;
;             if (last && has_next) S.a_ready(nxt);
;             if constexpr (GATHER) { if (last) { if (has_next) { PG8_GREAD(vN, nxt, (ui + 1) & 1); } else { _Pragma("unroll") for (int h_ = 0; h_ < 2; ++h_) _Pragma("unroll") for (int i_ = 0; i_ < 2; ++i_) vN[h_][i_] = vC[h_][i_]; } } }
;             unsigned vS[2][2];
; #pragma unroll
;             for (int h_ = 0; h_ < 2; ++h_)
; #pragma unroll
;                 for (int i_ = 0; i_ < 2; ++i_) vS[h_][i_] = (GATHER && last) ? vN[h_][i_] : vC[h_][i_];
;             if constexpr (SP2) {
;             PG8_LDB(B0, 0, 0); PG8_LDB(B1, 0, 1); PG8_SCHED; PG8_LDA(At, 0, 0); PG8_STAGE(PG8_SA(1, 1), a1 + PG8_AH(1), PG8_VA(vC, 1));
;             PG8_WAIT_V(8); PG8_WAIT_L(0); PG8_BAR; PG8_MMA(0, 0, At, B0); PG8_MMA(0, 1, At, B1); PG8_BAR; PG8_SCHED;
;             PG8_LDA(At, 0, 1); PG8_STAGE(PG8_SB(0, 0), b2, voffB); PG8_STAGE(PG8_SB(0, 1), b2 + hstep, voffB); PG8_STAGE(PG8_SA(0, 0), a2, PG8_VA(vS, 0));
.LBB0_1174:
	s_add_u32 s2, s12, 0xfffc0080
	s_addc_u32 s10, s13, -1
	s_cmp_eq_u32 s67, 12
	s_cselect_b32 s15, s7, s10
	s_cselect_b32 s14, s9, s2
	s_cselect_b32 s11, s18, s29
	s_cselect_b32 s10, s19, s27
	s_add_i32 s2, 0, 0x10000
	s_add_i32 s70, 0, 0x14000
	v_add_u32_e32 v78, s2, v168
	v_add_u32_e32 v164, s70, v168
	ds_read_b128 v[66:69], v78
	ds_read_b128 v[70:73], v78 offset:1024
	ds_read_b128 v[74:77], v78 offset:2048
	ds_read_b128 v[78:81], v78 offset:3072
	ds_read_b128 v[156:159], v164
	ds_read_b128 v[160:163], v164 offset:1024
	ds_read_b128 v[172:175], v164 offset:2048
	ds_read_b128 v[176:179], v164 offset:3072
	v_lshl_add_u64 v[164:165], s[12:13], 0, v[152:153]
	s_add_i32 m0, s47, 0xc000
	ds_read_b128 v[180:183], v170
	ds_read_b128 v[184:187], v170 offset:1024
	ds_read_b128 v[188:191], v170 offset:2048
	ds_read_b128 v[192:195], v170 offset:3072
	ds_read_b128 v[196:199], v170 offset:4096
	ds_read_b128 v[200:203], v170 offset:5120
	ds_read_b128 v[204:207], v170 offset:6144
	ds_read_b128 v[208:211], v170 offset:7168
	global_load_lds_dwordx4 v[164:165], off
	v_lshl_add_u64 v[164:165], s[12:13], 0, v[154:155]
	s_add_i32 m0, s47, 0xe000
	s_nop 0
	global_load_lds_dwordx4 v[164:165], off
	s_waitcnt vmcnt(8)
	s_waitcnt lgkmcnt(0)
	s_barrier
	s_setprio 1
	v_mfma_f32_16x16x32_bf16 v[142:145], v[66:69], v[180:183], v[142:145]
	v_mfma_f32_16x16x32_bf16 v[138:141], v[74:77], v[180:183], v[138:141]
	v_mfma_f32_16x16x32_bf16 v[126:129], v[66:69], v[188:191], v[126:129]
	v_mfma_f32_16x16x32_bf16 v[122:125], v[74:77], v[188:191], v[122:125]
	v_mfma_f32_16x16x32_bf16 v[110:113], v[66:69], v[196:199], v[110:113]
	v_mfma_f32_16x16x32_bf16 v[106:109], v[74:77], v[196:199], v[106:109]
	v_mfma_f32_16x16x32_bf16 v[94:97], v[66:69], v[204:207], v[94:97]
	v_mfma_f32_16x16x32_bf16 v[90:93], v[74:77], v[204:207], v[90:93]
	v_mfma_f32_16x16x32_bf16 v[142:145], v[70:73], v[184:187], v[142:145]
	v_mfma_f32_16x16x32_bf16 v[138:141], v[78:81], v[184:187], v[138:141]
	v_mfma_f32_16x16x32_bf16 v[126:129], v[70:73], v[192:195], v[126:129]
	v_mfma_f32_16x16x32_bf16 v[122:125], v[78:81], v[192:195], v[122:125]
	v_mfma_f32_16x16x32_bf16 v[110:113], v[70:73], v[200:203], v[110:113]
	v_mfma_f32_16x16x32_bf16 v[106:109], v[78:81], v[200:203], v[106:109]
	v_mfma_f32_16x16x32_bf16 v[94:97], v[70:73], v[208:211], v[94:97]
	v_mfma_f32_16x16x32_bf16 v[90:93], v[78:81], v[208:211], v[90:93]
	v_mfma_f32_16x16x32_bf16 v[134:137], v[156:159], v[180:183], v[134:137]
	v_mfma_f32_16x16x32_bf16 v[130:133], v[172:175], v[180:183], v[130:133]
	v_mfma_f32_16x16x32_bf16 v[118:121], v[156:159], v[188:191], v[118:121]
	v_mfma_f32_16x16x32_bf16 v[114:117], v[172:175], v[188:191], v[114:117]
	v_mfma_f32_16x16x32_bf16 v[102:105], v[156:159], v[196:199], v[102:105]
	v_mfma_f32_16x16x32_bf16 v[98:101], v[172:175], v[196:199], v[98:101]
	v_mfma_f32_16x16x32_bf16 v[86:89], v[156:159], v[204:207], v[86:89]
	v_mfma_f32_16x16x32_bf16 v[82:85], v[172:175], v[204:207], v[82:85]
	v_mfma_f32_16x16x32_bf16 v[134:137], v[160:163], v[184:187], v[134:137]
	v_mfma_f32_16x16x32_bf16 v[130:133], v[176:179], v[184:187], v[130:133]
	v_mfma_f32_16x16x32_bf16 v[118:121], v[160:163], v[192:195], v[118:121]
	v_mfma_f32_16x16x32_bf16 v[114:117], v[176:179], v[192:195], v[114:117]
	v_mfma_f32_16x16x32_bf16 v[102:105], v[160:163], v[200:203], v[102:105]
	v_mfma_f32_16x16x32_bf16 v[98:101], v[176:179], v[200:203], v[98:101]
	v_mfma_f32_16x16x32_bf16 v[86:89], v[160:163], v[208:211], v[86:89]
	v_mfma_f32_16x16x32_bf16 v[82:85], v[176:179], v[208:211], v[82:85]
	s_setprio 0
	s_barrier
	s_add_i32 s2, s2, s45
	v_lshl_add_u64 v[164:165], s[10:11], 0, v[0:1]
	s_mov_b32 m0, s2
	ds_read_b128 v[180:183], v170 offset:16384
	ds_read_b128 v[184:187], v170 offset:17408
	ds_read_b128 v[188:191], v170 offset:18432
	ds_read_b128 v[192:195], v170 offset:19456
	ds_read_b128 v[196:199], v170 offset:20480
	ds_read_b128 v[200:203], v170 offset:21504
	ds_read_b128 v[204:207], v170 offset:22528
	ds_read_b128 v[208:211], v170 offset:23552
	global_load_lds_dwordx4 v[164:165], off
	s_add_i32 m0, s2, 0x2000
	s_add_u32 s68, s10, 0x40000
	v_lshl_add_u64 v[212:213], s[10:11], 0, v[146:147]
	s_addc_u32 s69, s11, 0
	s_add_i32 s2, s70, s45
	global_load_lds_dwordx4 v[212:213], off
	v_lshl_add_u64 v[214:215], s[68:69], 0, v[0:1]
	s_mov_b32 m0, s2
	v_lshl_add_u64 v[216:217], s[14:15], 0, v[148:149]
	global_load_lds_dwordx4 v[214:215], off
	v_lshl_add_u64 v[214:215], s[68:69], 0, v[146:147]
	s_add_i32 m0, s2, 0x2000
	s_nop 0
	global_load_lds_dwordx4 v[214:215], off
	v_lshl_add_u64 v[214:215], s[14:15], 0, v[150:151]
	s_mov_b32 m0, s47
	s_nop 0
	global_load_lds_dwordx4 v[214:215], off
	s_mov_b32 m0, s50
	s_nop 0
	global_load_lds_dwordx4 v[216:217], off
	s_waitcnt vmcnt(8)
	s_waitcnt lgkmcnt(0)
	s_barrier
; #define PG8_STAGE(bufoff, gbase, voff) do { _Pragma("unroll") for (int _i = 0; _i < 2; ++_i) \
;         __builtin_amdgcn_global_load_lds((const unsigned*)((const char*)(gbase) + (voff)[_i]), (PG8_LAS unsigned*)(lds + (bufoff) + ldsw + _i * 8192), 16, 0, 0); } while (0)
; #define PG8_LDA(dst, b, h) do { _Pragma("unroll") for (int m = 0; m < 4; ++m) _Pragma("unroll") for (int k = 0; k < 2; ++k) dst[m][k] = *(const PG8_LAS bf16x8*)(lds + PG8_SA(b, h) + aoff + m * 2048 + k * 1024); } while (0)
; #define PG8_LDB(dst, b, h) do { _Pragma("unroll") for (int n = 0; n < 2; ++n) _Pragma("unroll") for (int k = 0; k < 2; ++k) dst[n][k] = *(const PG8_LAS bf16x8*)(lds + PG8_SB(b, h) + boff + n * 2048 + k * 1024); } while (0)
; #define PG8_MMA(ai, bj, At, Bt) do { __builtin_amdgcn_s_setprio(1); _Pragma("unroll") for (int m = 0; m < 4; ++m) _Pragma("unroll") for (int n = 0; n < 2; ++n) _Pragma("unroll") for (int k = 0; k < 2; ++k) \
;         acc[ai][bj][m][n] = __builtin_amdgcn_mfma_f32_16x16x32_bf16(Bt[n][k], At[m][k], acc[ai][bj][m][n], 0, 0, 0); __builtin_amdgcn_s_setprio(0); } while (0)
; #define PG8_WAIT_V(n) asm volatile("s_waitcnt vmcnt(" #n ")" ::: "memory")
; #define PG8_WAIT_L(n) asm volatile("s_waitcnt lgkmcnt(" #n ")" ::: "memory")
; #define PG8_BAR __builtin_amdgcn_s_barrier()
; #define PG8_SCHED __builtin_amdgcn_sched_barrier(0)
; template <class Epi, class Sched, bool ALIGN_EPI = false, bool SP2 = false, bool GATHER = false>
; __device__ __forceinline__ void gemm_phase(PG8_LAS unsigned char* lds, const Gemm g, const Sched& S, const Epi& E, const int2* gslot = nullptr, PG8_LAS unsigned char* gtab = nullptr) {
;     ...
;             PG8_LDA(At, 0, 1); PG8_STAGE(PG8_SB(0, 0), b2, voffB); PG8_STAGE(PG8_SB(0, 1), b2 + hstep, voffB); PG8_STAGE(PG8_SA(0, 0), a2, PG8_VA(vS, 0));
;             PG8_WAIT_V(8); PG8_WAIT_L(0); PG8_BAR; PG8_MMA(1, 0, At, B0); PG8_MMA(1, 1, At, B1); PG8_BAR; PG8_SCHED;
;             PG8_LDB(B0, 1, 0); PG8_LDB(B1, 1, 1); PG8_SCHED; PG8_LDA(At, 1, 0); PG8_STAGE(PG8_SA(0, 1), a2 + PG8_AH(1), PG8_VA(vS, 1));
;             PG8_WAIT_V(8); PG8_WAIT_L(0); PG8_BAR; PG8_MMA(0, 0, At, B0); PG8_MMA(0, 1, At, B1); PG8_BAR; PG8_SCHED;
	s_setprio 1
	v_mfma_f32_16x16x32_bf16 v[62:65], v[66:69], v[180:183], v[62:65]
	v_mfma_f32_16x16x32_bf16 v[58:61], v[74:77], v[180:183], v[58:61]
	v_mfma_f32_16x16x32_bf16 v[46:49], v[66:69], v[188:191], v[46:49]
	v_mfma_f32_16x16x32_bf16 v[42:45], v[74:77], v[188:191], v[42:45]
	v_mfma_f32_16x16x32_bf16 v[30:33], v[66:69], v[196:199], v[30:33]
	v_mfma_f32_16x16x32_bf16 v[26:29], v[74:77], v[196:199], v[26:29]
	v_mfma_f32_16x16x32_bf16 v[14:17], v[66:69], v[204:207], v[14:17]
	v_mfma_f32_16x16x32_bf16 v[10:13], v[74:77], v[204:207], v[10:13]
	v_mfma_f32_16x16x32_bf16 v[62:65], v[70:73], v[184:187], v[62:65]
	v_mfma_f32_16x16x32_bf16 v[58:61], v[78:81], v[184:187], v[58:61]
	v_mfma_f32_16x16x32_bf16 v[46:49], v[70:73], v[192:195], v[46:49]
	v_mfma_f32_16x16x32_bf16 v[42:45], v[78:81], v[192:195], v[42:45]
	v_mfma_f32_16x16x32_bf16 v[30:33], v[70:73], v[200:203], v[30:33]
	v_mfma_f32_16x16x32_bf16 v[26:29], v[78:81], v[200:203], v[26:29]
	v_mfma_f32_16x16x32_bf16 v[14:17], v[70:73], v[208:211], v[14:17]
	v_mfma_f32_16x16x32_bf16 v[10:13], v[78:81], v[208:211], v[10:13]
	v_mfma_f32_16x16x32_bf16 v[54:57], v[156:159], v[180:183], v[54:57]
	v_mfma_f32_16x16x32_bf16 v[50:53], v[172:175], v[180:183], v[50:53]
	v_mfma_f32_16x16x32_bf16 v[38:41], v[156:159], v[188:191], v[38:41]
	v_mfma_f32_16x16x32_bf16 v[34:37], v[172:175], v[188:191], v[34:37]
	v_mfma_f32_16x16x32_bf16 v[22:25], v[156:159], v[196:199], v[22:25]
	v_mfma_f32_16x16x32_bf16 v[18:21], v[172:175], v[196:199], v[18:21]
	v_mfma_f32_16x16x32_bf16 v[6:9], v[156:159], v[204:207], v[6:9]
	v_mfma_f32_16x16x32_bf16 v[2:5], v[172:175], v[204:207], v[2:5]
	v_mfma_f32_16x16x32_bf16 v[54:57], v[160:163], v[184:187], v[54:57]
	v_mfma_f32_16x16x32_bf16 v[50:53], v[176:179], v[184:187], v[50:53]
	v_mfma_f32_16x16x32_bf16 v[38:41], v[160:163], v[192:195], v[38:41]
	v_mfma_f32_16x16x32_bf16 v[34:37], v[176:179], v[192:195], v[34:37]
	v_mfma_f32_16x16x32_bf16 v[22:25], v[160:163], v[200:203], v[22:25]
	v_mfma_f32_16x16x32_bf16 v[18:21], v[176:179], v[200:203], v[18:21]
	v_mfma_f32_16x16x32_bf16 v[6:9], v[160:163], v[208:211], v[6:9]
	v_mfma_f32_16x16x32_bf16 v[2:5], v[176:179], v[208:211], v[2:5]
	s_setprio 0
	s_barrier
	s_add_i32 s2, 0, 0x18000
	s_add_i32 s68, 0, 0x1c000
	v_add_u32_e32 v78, s2, v168
	v_add_u32_e32 v171, s68, v168
	ds_read_b128 v[66:69], v78
	ds_read_b128 v[70:73], v78 offset:1024
	ds_read_b128 v[74:77], v78 offset:2048
	ds_read_b128 v[78:81], v78 offset:3072
	ds_read_b128 v[156:159], v171
	ds_read_b128 v[160:163], v171 offset:1024
	ds_read_b128 v[172:175], v171 offset:2048
	ds_read_b128 v[176:179], v171 offset:3072
	s_add_u32 s14, s14, 0x40000
	s_addc_u32 s15, s15, 0
	s_mov_b32 m0, s51
	v_lshl_add_u64 v[218:219], s[14:15], 0, v[150:151]
	ds_read_b128 v[180:183], v170 offset:32768
	ds_read_b128 v[184:187], v170 offset:33792
	ds_read_b128 v[188:191], v170 offset:34816
	ds_read_b128 v[192:195], v170 offset:35840
	ds_read_b128 v[196:199], v170 offset:36864
	ds_read_b128 v[200:203], v170 offset:37888
	ds_read_b128 v[204:207], v170 offset:38912
	ds_read_b128 v[208:211], v170 offset:39936
	global_load_lds_dwordx4 v[218:219], off
	v_lshl_add_u64 v[218:219], s[14:15], 0, v[148:149]
	s_mov_b32 m0, s52
	s_nop 0
	global_load_lds_dwordx4 v[218:219], off
	s_waitcnt vmcnt(8)
	s_waitcnt lgkmcnt(0)
	s_barrier
	s_setprio 1
	v_mfma_f32_16x16x32_bf16 v[142:145], v[66:69], v[180:183], v[142:145]
	v_mfma_f32_16x16x32_bf16 v[138:141], v[74:77], v[180:183], v[138:141]
	v_mfma_f32_16x16x32_bf16 v[126:129], v[66:69], v[188:191], v[126:129]
	v_mfma_f32_16x16x32_bf16 v[122:125], v[74:77], v[188:191], v[122:125]
	v_mfma_f32_16x16x32_bf16 v[110:113], v[66:69], v[196:199], v[110:113]
	v_mfma_f32_16x16x32_bf16 v[106:109], v[74:77], v[196:199], v[106:109]
	v_mfma_f32_16x16x32_bf16 v[94:97], v[66:69], v[204:207], v[94:97]
	v_mfma_f32_16x16x32_bf16 v[90:93], v[74:77], v[204:207], v[90:93]
	v_mfma_f32_16x16x32_bf16 v[142:145], v[70:73], v[184:187], v[142:145]
	v_mfma_f32_16x16x32_bf16 v[138:141], v[78:81], v[184:187], v[138:141]
	v_mfma_f32_16x16x32_bf16 v[126:129], v[70:73], v[192:195], v[126:129]
	v_mfma_f32_16x16x32_bf16 v[122:125], v[78:81], v[192:195], v[122:125]
	v_mfma_f32_16x16x32_bf16 v[110:113], v[70:73], v[200:203], v[110:113]
	v_mfma_f32_16x16x32_bf16 v[106:109], v[78:81], v[200:203], v[106:109]
	v_mfma_f32_16x16x32_bf16 v[94:97], v[70:73], v[208:211], v[94:97]
	v_mfma_f32_16x16x32_bf16 v[90:93], v[78:81], v[208:211], v[90:93]
	v_mfma_f32_16x16x32_bf16 v[134:137], v[156:159], v[180:183], v[134:137]
	v_mfma_f32_16x16x32_bf16 v[130:133], v[172:175], v[180:183], v[130:133]
	v_mfma_f32_16x16x32_bf16 v[118:121], v[156:159], v[188:191], v[118:121]
	v_mfma_f32_16x16x32_bf16 v[114:117], v[172:175], v[188:191], v[114:117]
	v_mfma_f32_16x16x32_bf16 v[102:105], v[156:159], v[196:199], v[102:105]
	v_mfma_f32_16x16x32_bf16 v[98:101], v[172:175], v[196:199], v[98:101]
	v_mfma_f32_16x16x32_bf16 v[86:89], v[156:159], v[204:207], v[86:89]
	v_mfma_f32_16x16x32_bf16 v[82:85], v[172:175], v[204:207], v[82:85]
	v_mfma_f32_16x16x32_bf16 v[134:137], v[160:163], v[184:187], v[134:137]
	v_mfma_f32_16x16x32_bf16 v[130:133], v[176:179], v[184:187], v[130:133]
	v_mfma_f32_16x16x32_bf16 v[118:121], v[160:163], v[192:195], v[118:121]
	v_mfma_f32_16x16x32_bf16 v[114:117], v[176:179], v[192:195], v[114:117]
	v_mfma_f32_16x16x32_bf16 v[102:105], v[160:163], v[200:203], v[102:105]
	v_mfma_f32_16x16x32_bf16 v[98:101], v[176:179], v[200:203], v[98:101]
	v_mfma_f32_16x16x32_bf16 v[86:89], v[160:163], v[208:211], v[86:89]
	v_mfma_f32_16x16x32_bf16 v[82:85], v[176:179], v[208:211], v[82:85]
	s_setprio 0
	s_barrier
; #define PG8_STAGE(bufoff, gbase, voff) do { _Pragma("unroll") for (int _i = 0; _i < 2; ++_i) \
;         __builtin_amdgcn_global_load_lds((const unsigned*)((const char*)(gbase) + (voff)[_i]), (PG8_LAS unsigned*)(lds + (bufoff) + ldsw + _i * 8192), 16, 0, 0); } while (0)
; #define PG8_LDA(dst, b, h) do { _Pragma("unroll") for (int m = 0; m < 4; ++m) _Pragma("unroll") for (int k = 0; k < 2; ++k) dst[m][k] = *(const PG8_LAS bf16x8*)(lds + PG8_SA(b, h) + aoff + m * 2048 + k * 1024); } while (0)
; #define PG8_MMA(ai, bj, At, Bt) do { __builtin_amdgcn_s_setprio(1); _Pragma("unroll") for (int m = 0; m < 4; ++m) _Pragma("unroll") for (int n = 0; n < 2; ++n) _Pragma("unroll") for (int k = 0; k < 2; ++k) \
;         acc[ai][bj][m][n] = __builtin_amdgcn_mfma_f32_16x16x32_bf16(Bt[n][k], At[m][k], acc[ai][bj][m][n], 0, 0, 0); __builtin_amdgcn_s_setprio(0); } while (0)
; #define PG8_WAIT_V(n) asm volatile("s_waitcnt vmcnt(" #n ")" ::: "memory")
; #define PG8_WAIT_L(n) asm volatile("s_waitcnt lgkmcnt(" #n ")" ::: "memory")
; #define PG8_BAR __builtin_amdgcn_s_barrier()
; #define PG8_SCHED __builtin_amdgcn_sched_barrier(0)
; template <class Epi, class Sched, bool ALIGN_EPI = false, bool SP2 = false, bool GATHER = false>
; __device__ __forceinline__ void gemm_phase(PG8_LAS unsigned char* lds, const Gemm g, const Sched& S, const Epi& E, const int2* gslot = nullptr, PG8_LAS unsigned char* gtab = nullptr) {
;     ...
;             PG8_LDA(At, 1, 1); PG8_STAGE(PG8_SB(1, 0), b3, voffB); PG8_STAGE(PG8_SB(1, 1), b3 + hstep, voffB); PG8_STAGE(PG8_SA(1, 0), a3, PG8_VA(vS, 0));
;             PG8_WAIT_V(8); PG8_WAIT_L(0); PG8_BAR; PG8_MMA(1, 0, At, B0); PG8_MMA(1, 1, At, B1); PG8_BAR; PG8_SCHED;
;     ...
;         if constexpr (ALIGN_EPI) { if (wr == 0) PG8_BAR; }
	s_add_i32 s2, s2, s45
	v_lshl_add_u64 v[164:165], v[164:165], 0, s[54:55]
	s_mov_b32 m0, s2
	ds_read_b128 v[180:183], v170 offset:49152
	ds_read_b128 v[184:187], v170 offset:50176
	ds_read_b128 v[188:191], v170 offset:51200
	ds_read_b128 v[192:195], v170 offset:52224
	ds_read_b128 v[196:199], v170 offset:53248
	ds_read_b128 v[200:203], v170 offset:54272
	ds_read_b128 v[204:207], v170 offset:55296
	ds_read_b128 v[208:211], v170 offset:56320
	global_load_lds_dwordx4 v[164:165], off
	s_add_i32 m0, s2, 0x2000
	s_add_u32 s10, s10, 0x40080
	v_lshl_add_u64 v[164:165], v[212:213], 0, s[54:55]
	s_addc_u32 s11, s11, 0
	s_add_i32 s2, s68, s45
	global_load_lds_dwordx4 v[164:165], off
	v_lshl_add_u64 v[164:165], s[10:11], 0, v[0:1]
	s_mov_b32 m0, s2
	s_nop 0
	global_load_lds_dwordx4 v[164:165], off
	v_lshl_add_u64 v[164:165], s[10:11], 0, v[146:147]
	s_add_i32 m0, s2, 0x2000
	s_nop 0
	global_load_lds_dwordx4 v[164:165], off
	v_lshl_add_u64 v[164:165], v[214:215], 0, s[54:55]
	s_mov_b32 m0, s58
	s_nop 0
	global_load_lds_dwordx4 v[164:165], off
	v_lshl_add_u64 v[164:165], v[216:217], 0, s[54:55]
	s_mov_b32 m0, s59
	s_nop 0
	global_load_lds_dwordx4 v[164:165], off
	s_waitcnt vmcnt(8)
	s_waitcnt lgkmcnt(0)
	s_barrier
	s_setprio 1
	v_mfma_f32_16x16x32_bf16 v[62:65], v[66:69], v[180:183], v[62:65]
	v_mfma_f32_16x16x32_bf16 v[58:61], v[74:77], v[180:183], v[58:61]
	v_mfma_f32_16x16x32_bf16 v[46:49], v[66:69], v[188:191], v[46:49]
	v_mfma_f32_16x16x32_bf16 v[42:45], v[74:77], v[188:191], v[42:45]
	v_mfma_f32_16x16x32_bf16 v[30:33], v[66:69], v[196:199], v[30:33]
	v_mfma_f32_16x16x32_bf16 v[26:29], v[74:77], v[196:199], v[26:29]
	v_mfma_f32_16x16x32_bf16 v[14:17], v[66:69], v[204:207], v[14:17]
	v_mfma_f32_16x16x32_bf16 v[10:13], v[74:77], v[204:207], v[10:13]
	v_mfma_f32_16x16x32_bf16 v[62:65], v[70:73], v[184:187], v[62:65]
	v_mfma_f32_16x16x32_bf16 v[58:61], v[78:81], v[184:187], v[58:61]
	v_mfma_f32_16x16x32_bf16 v[46:49], v[70:73], v[192:195], v[46:49]
	v_mfma_f32_16x16x32_bf16 v[42:45], v[78:81], v[192:195], v[42:45]
	v_mfma_f32_16x16x32_bf16 v[30:33], v[70:73], v[200:203], v[30:33]
	v_mfma_f32_16x16x32_bf16 v[26:29], v[78:81], v[200:203], v[26:29]
	v_mfma_f32_16x16x32_bf16 v[14:17], v[70:73], v[208:211], v[14:17]
	v_mfma_f32_16x16x32_bf16 v[10:13], v[78:81], v[208:211], v[10:13]
	v_mfma_f32_16x16x32_bf16 v[54:57], v[156:159], v[180:183], v[54:57]
	v_mfma_f32_16x16x32_bf16 v[50:53], v[172:175], v[180:183], v[50:53]
	v_mfma_f32_16x16x32_bf16 v[38:41], v[156:159], v[188:191], v[38:41]
	v_mfma_f32_16x16x32_bf16 v[34:37], v[172:175], v[188:191], v[34:37]
	v_mfma_f32_16x16x32_bf16 v[22:25], v[156:159], v[196:199], v[22:25]
	v_mfma_f32_16x16x32_bf16 v[18:21], v[172:175], v[196:199], v[18:21]
	v_mfma_f32_16x16x32_bf16 v[6:9], v[156:159], v[204:207], v[6:9]
	v_mfma_f32_16x16x32_bf16 v[2:5], v[172:175], v[204:207], v[2:5]
	v_mfma_f32_16x16x32_bf16 v[54:57], v[160:163], v[184:187], v[54:57]
	v_mfma_f32_16x16x32_bf16 v[50:53], v[176:179], v[184:187], v[50:53]
	v_mfma_f32_16x16x32_bf16 v[38:41], v[160:163], v[192:195], v[38:41]
	v_mfma_f32_16x16x32_bf16 v[34:37], v[176:179], v[192:195], v[34:37]
	v_mfma_f32_16x16x32_bf16 v[22:25], v[160:163], v[200:203], v[22:25]
	v_mfma_f32_16x16x32_bf16 v[18:21], v[176:179], v[200:203], v[18:21]
	v_mfma_f32_16x16x32_bf16 v[6:9], v[160:163], v[208:211], v[6:9]
	v_mfma_f32_16x16x32_bf16 v[2:5], v[176:179], v[208:211], v[2:5]
	s_setprio 0
	s_barrier
	s_add_i32 s67, s67, 2
	s_add_u32 s12, s12, 0x100
	s_addc_u32 s13, s13, 0
	s_add_u32 s27, s27, 0x100
	s_addc_u32 s29, s29, 0
	s_cmp_gt_u32 s67, 13
	s_cbranch_scc0 .LBB0_1174
	s_and_b64 vcc, exec, s[24:25]
	s_cbranch_vccz .LBB0_1177
	s_barrier
